# MLA fixed-shift fast softmax v3: original tile code minus max chain and subs, per-unit l guard with WG-uniform redo in online-softmax mode
# speedup vs baseline: 1.0135x; 1.0040x over previous
.LBB0_1210:
	s_cmp_lt_i32 s44, 4
	s_cselect_b64 s[42:43], -1, 0
	s_and_b64 s[0:1], s[42:43], s[6:7]
	s_andn2_b64 vcc, exec, s[0:1]
	s_cbranch_vccnz .LBB0_1343
	v_readlane_b32 s0, v251, 2
	v_mov_b32_e32 v181, 0
	v_mov_b32_e32 v0, 0
	s_mov_b64 s[6:7], s[62:63]
	s_cmpk_gt_i32 s0, 0xff
	s_cbranch_scc1 .LBB0_1343
	s_mov_b32 s99, 0
	v_writelane_b32 v251, s42, 22
	s_mul_i32 s8, s46, 12
	s_add_i32 s11, s8, 11
	v_writelane_b32 v251, s43, 23
	v_writelane_b32 v251, s50, 24
	s_add_i32 s9, s8, 10
	s_lshr_b32 s12, s11, 4
	v_writelane_b32 v251, s51, 25
	v_writelane_b32 v251, s48, 26
	s_lshr_b32 s10, s9, 4
	s_lshl_b32 s0, s12, 14
	v_writelane_b32 v251, s49, 27
	s_lshl_b32 s2, s10, 14
	s_add_i32 s3, s0, 0xc000
	v_readlane_b32 s19, v251, 5
	s_cmpk_lt_u32 s19, 0x180
	s_cselect_b64 s[0:1], -1, 0
	s_and_b64 s[0:1], s[0:1], exec
	s_cselect_b32 s0, s3, 0x20400
	s_add_i32 s1, s2, 0xc000
	s_cmpk_lt_u32 s19, 0x180
	s_cselect_b64 s[2:3], -1, 0
	s_and_b64 s[2:3], s[2:3], exec
	s_cselect_b32 s1, s1, 0x20400
	s_add_i32 s13, s8, 9
	s_lshr_b32 s14, s13, 4
	s_lshl_b32 s2, s14, 14
	s_add_i32 s4, s2, 0xc000
	s_cmpk_lt_u32 s19, 0x180
	s_cselect_b64 s[2:3], -1, 0
	s_and_b64 s[2:3], s[2:3], exec
	s_cselect_b32 s2, s4, 0x20400
	s_add_i32 s15, s8, 8
	s_lshr_b32 s16, s15, 4
	s_lshl_b32 s3, s16, 14
	v_writelane_b32 v251, s6, 28
	s_load_dwordx2 s[4:5], s[6:7], 0xb0
	s_add_i32 s3, s3, 0xc000
	s_cmpk_lt_u32 s19, 0x180
	s_cselect_b64 s[20:21], -1, 0
	v_writelane_b32 v251, s7, 29
	s_and_b64 s[6:7], s[20:21], exec
	s_cselect_b32 s3, s3, 0x20400
	s_waitcnt lgkmcnt(0)
	s_add_u32 s6, s4, 0xae00000
	v_writelane_b32 v251, s6, 30
	s_addc_u32 s6, s5, 0
	v_writelane_b32 v251, s6, 31
	s_add_u32 s6, s4, 0xa800000
	v_writelane_b32 v251, s6, 32
	s_addc_u32 s6, s5, 0
	v_writelane_b32 v251, s6, 33
	s_add_u32 s6, s4, 0xac00000
	v_writelane_b32 v251, s6, 34
	s_addc_u32 s6, s5, 0
	v_writelane_b32 v251, s6, 35
	s_add_u32 s6, s4, 0x1100000
	v_writelane_b32 v251, s6, 36
	s_addc_u32 s6, s5, 0
	v_writelane_b32 v251, s6, 37
	s_add_u32 s6, s4, 0xa000000
	v_writelane_b32 v251, s6, 38
	s_addc_u32 s6, s5, 0
	v_writelane_b32 v251, s6, 39
	s_add_u32 s6, s4, 0x100000
	v_writelane_b32 v251, s6, 43
	s_addc_u32 s6, s5, 0
	s_add_u32 s34, s4, 0x1000000
	s_addc_u32 s35, s5, 0
	v_writelane_b32 v251, s6, 45
	s_add_u32 s6, s4, 0x400000
	v_writelane_b32 v251, s6, 47
	s_addc_u32 s6, s5, 0
	v_writelane_b32 v251, s6, 48
	s_lshl_b32 s6, s46, 13
	s_or_b32 s7, s6, 0x18000
	s_and_b32 s6, s6, 0x2000
	s_or_b32 s6, s6, 0x20400
	s_cmpk_lt_u32 s19, 0x100
	s_cselect_b32 s6, s7, s6
	s_add_i32 s40, s6, 0
	v_readlane_b32 s6, v251, 20
	v_readlane_b32 s7, v251, 21
	v_writelane_b32 v251, s20, 49
	s_and_b64 s[6:7], s[6:7], s[20:21]
	s_lshl_b32 s23, s46, 5
	v_writelane_b32 v251, s21, 50
	v_writelane_b32 v251, s6, 51
	v_mbcnt_lo_u32_b32 v0, -1, v0
	v_mbcnt_hi_u32_b32 v0, -1, v0
	v_writelane_b32 v251, s7, 52
	s_add_u32 s6, s4, 0x1400000
	v_writelane_b32 v251, s6, 53
	s_addc_u32 s6, s5, 0
	s_add_u32 s4, s4, 0x800000
	v_writelane_b32 v251, s6, 54
	s_addc_u32 s5, s5, 0
	v_writelane_b32 v251, s4, 55
	s_and_b32 s20, s8, 4
	v_and_b32_e32 v183, 63, v0
	v_writelane_b32 v251, s5, 56
	s_lshl_b32 s4, s46, 10
	s_add_i32 s88, s4, 0
	s_mul_i32 s4, s46, 24
	s_lshr_b32 s5, s8, 4
	s_and_b32 s6, s4, 24
	s_lshl_b32 s7, s5, 5
	s_lshl_b32 s4, s5, 14
	s_lshl_b32 s5, s6, 9
	s_add_i32 s22, s5, 0
	s_or_b32 s5, s6, 2
	v_writelane_b32 v251, s5, 57
	s_lshl_b32 s5, s5, 9
	s_add_i32 s74, s5, 0
	s_or_b32 s5, s20, s7
	s_or_b32 s17, s6, 4
	v_writelane_b32 v251, s7, 59
	s_or_b32 s5, s5, 8
	v_writelane_b32 v251, s5, 60
	s_lshl_b32 s5, s17, 9
	s_add_i32 s76, s5, 0
	s_or_b32 s5, s6, 6
	v_writelane_b32 v250, s5, 0
	s_lshl_b32 s5, s5, 9
	v_writelane_b32 v251, s17, 61
	s_add_i32 s78, s5, 0
	s_add_i32 s5, s8, 4
	v_writelane_b32 v251, s6, 63
	s_lshl_b32 s6, s5, 1
	s_lshr_b32 s7, s5, 4
	s_add_i32 s4, s4, 0xc000
	s_and_b32 s6, s6, 24
	s_lshl_b32 s17, s7, 5
	s_and_b32 s5, s5, 4
	v_writelane_b32 v250, s17, 1
	s_cmpk_lt_u32 s19, 0x140
	v_writelane_b32 v250, s5, 3
	s_cselect_b64 s[24:25], -1, 0
	v_writelane_b32 v250, s24, 4
	s_lshl_b32 s5, s7, 14
	s_lshl_b32 s15, s15, 1
	v_writelane_b32 v250, s25, 5
	v_writelane_b32 v250, s6, 6
	s_lshl_b32 s6, s6, 9
	s_add_i32 s94, s6, 0
	s_add_i32 s6, s8, 5
	s_lshr_b32 s17, s6, 4
	s_lshl_b32 s18, s17, 5
	s_lshl_b32 s7, s6, 1
	v_writelane_b32 v250, s18, 7
	s_and_b32 s6, s6, 4
	s_and_b32 s7, s7, 26
	v_writelane_b32 v250, s6, 8
	v_writelane_b32 v250, s7, 9
	s_lshl_b32 s7, s7, 9
	s_add_i32 s24, s7, 0
	s_add_i32 s7, s8, 6
	s_lshl_b32 s6, s17, 14
	s_lshl_b32 s17, s7, 1
	s_lshr_b32 s18, s7, 4
	s_and_b32 s21, s17, 28
	s_lshl_b32 s17, s18, 5
	s_and_b32 s7, s7, 4
	v_writelane_b32 v250, s7, 11
	s_or_b32 s7, s17, 8
	s_lshl_b32 s17, s21, 9
	s_add_i32 s8, s8, 7
	v_writelane_b32 v250, s7, 12
	s_lshl_b32 s7, s18, 14
	s_add_i32 s28, s17, 0
	s_lshl_b32 s17, s8, 1
	s_lshr_b32 s18, s8, 4
	s_mov_b32 s73, s21
	s_and_b32 s21, s17, 30
	s_lshl_b32 s17, s18, 5
	s_and_b32 s8, s8, 4
	v_writelane_b32 v250, s8, 13
	s_or_b32 s8, s17, 8
	s_lshl_b32 s17, s21, 9
	v_writelane_b32 v250, s8, 14
	s_add_i32 s90, s17, 0
	s_and_b32 s17, s15, 24
	s_lshl_b32 s15, s16, 5
	v_writelane_b32 v250, s20, 15
	s_or_b32 s15, s15, s20
	v_writelane_b32 v250, s15, 16
	s_lshl_b32 s15, s17, 9
	s_add_i32 s31, s15, 0
	s_lshl_b32 s15, s13, 1
	s_lshl_b32 s14, s14, 5
	s_and_b32 s15, s15, 26
	v_writelane_b32 v250, s14, 17
	s_and_b32 s13, s13, 4
	v_writelane_b32 v250, s13, 18
	s_lshl_b32 s13, s15, 9
	s_add_i32 s42, s13, 0
	s_lshl_b32 s13, s9, 1
	s_lshl_b32 s10, s10, 5
	s_and_b32 s9, s9, 4
	s_and_b32 s13, s13, 28
	v_writelane_b32 v250, s9, 19
	s_or_b32 s9, s10, 8
	v_writelane_b32 v250, s9, 20
	s_lshl_b32 s9, s13, 9
	s_add_i32 s87, s9, 0
	s_lshl_b32 s9, s11, 1
	s_and_b32 s10, s9, 30
	s_lshl_b32 s9, s12, 5
	s_and_b32 s11, s11, 4
	v_writelane_b32 v250, s11, 21
	s_or_b32 s9, s9, 8
	s_lshl_b32 s8, s18, 14
	v_writelane_b32 v250, s9, 23
	s_lshl_b32 s9, s10, 9
	s_add_i32 s5, s5, 0xc000
	s_add_i32 s6, s6, 0xc000
	s_add_i32 s7, s7, 0xc000
	s_add_i32 s8, s8, 0xc000
	s_mov_b32 s77, s10
	s_add_i32 s71, s9, 0
	v_readlane_b32 s10, v251, 3
	v_readlane_b32 s11, v251, 4
	s_add_u32 s9, s10, 0x1a000
	v_writelane_b32 v250, s9, 25
	s_addc_u32 s9, s11, 0
	s_cmpk_lt_u32 s19, 0x1c0
	s_cselect_b32 s4, s4, 0x20400
	v_writelane_b32 v250, s9, 26
	s_cselect_b32 s5, s5, 0x20400
	s_cselect_b32 s6, s6, 0x20400
	s_cselect_b32 s7, s7, 0x20400
	s_cselect_b32 s8, s8, 0x20400
	s_add_i32 s9, s22, s4
	s_add_i32 s74, s74, s4
	s_add_i32 s76, s76, s4
	s_add_i32 s78, s78, s4
	v_readlane_b32 s4, v251, 6
	v_bfe_u32 v190, v0, 3, 3
	v_and_b32_e32 v2, 7, v0
	v_or_b32_e32 v1, s4, v0
	v_lshrrev_b32_e32 v0, 1, v0
	v_lshlrev_b32_e32 v182, 3, v2
	v_lshlrev_b32_e32 v3, 10, v2
	v_lshlrev_b32_e32 v2, 2, v2
	v_and_b32_e32 v0, 12, v0
	v_add3_u32 v0, s40, v3, v0
	v_bitop3_b32 v3, v190, v2, 4 bitop3:0x6c
	v_or_b32_e32 v192, 8, v190
	v_lshl_add_u32 v191, v3, 2, v0
	v_bitop3_b32 v3, v192, v2, 12 bitop3:0x6c
	v_or_b32_e32 v194, 16, v190
	v_or_b32_e32 v196, 24, v190
	v_lshl_add_u32 v193, v3, 2, v0
	v_bitop3_b32 v3, v194, v2, 20 bitop3:0x6c
	v_bitop3_b32 v2, v196, v2, 28 bitop3:0x6c
	s_mov_b32 s72, s21
	s_mov_b32 s97, s17
	s_mov_b32 s41, s15
	s_mov_b32 s75, s13
	s_add_i32 s94, s94, s5
	s_add_i32 s24, s24, s6
	s_mov_b32 s22, 0x18000
	v_lshl_add_u32 v195, v3, 2, v0
	v_lshl_add_u32 v197, v2, 2, v0
	s_addk_i32 s40, 0xc00
	s_add_i32 s28, s28, s7
	s_mov_b32 s26, s23
	s_add_i32 s29, s23, 0xffffff85
	s_add_i32 s90, s90, s8
	s_mov_b32 s30, 0x2aaaaaab
	s_add_i32 s31, s31, s3
	s_movk_i32 s91, 0xffe8
	s_add_i32 s42, s42, s2
	s_add_i32 s86, s88, 0x4000
	s_add_i32 s87, s87, s1
	s_add_i32 s27, s88, 0x6000
	s_add_i32 s71, s71, s0
	s_add_i32 s38, s88, 0x8000
	v_mov_b32_e32 v198, 0x358637bd
	s_mov_b32 s23, 0x20000
	v_mov_b32_e32 v199, 0xff800000
	s_add_i32 s39, s88, 0xa000
	s_add_i32 s33, 0, 0x14000
	s_add_i32 s43, 0, 0x1c000
	s_mov_b32 s0, 0x41200000
	s_movk_i32 s1, 0x110
	v_readlane_b32 s5, v251, 2
	s_mov_b32 s45, 0
	v_cmp_eq_u32_e64 s[2:3], 0, v1
	v_writelane_b32 v250, s9, 27
	s_branch .LBB0_1214

.LBB0_1216:
	s_mov_b32 s100, s6
	s_waitcnt lgkmcnt(0)
	s_mul_i32 s6, s6, s54
	v_readlane_b32 s7, v251, 2
	s_add_i32 s6, s6, s7
	s_mul_i32 s8, s6, 6
	v_readlane_b32 s6, v251, 16
	s_add_i32 s8, s8, s6
	v_readlane_b32 s7, v251, 17
	s_cmpk_lt_i32 s8, 0xc00
	v_readlane_b32 s10, v251, 51
	s_cselect_b64 s[6:7], -1, 0
	v_readlane_b32 s11, v251, 52
	s_and_b64 s[62:63], s[10:11], s[6:7]
	s_andn2_b64 vcc, exec, s[62:63]
	s_mov_b64 s[6:7], -1
	s_cbranch_vccnz .LBB0_1221
	s_cmp_gt_i32 s8, -1
	s_cbranch_scc0 .LBB0_1219
	v_readlane_b32 s10, v251, 28
	v_readlane_b32 s11, v251, 29
	s_load_dwordx2 s[6:7], s[10:11], 0x78
	s_load_dwordx2 s[64:65], s[10:11], 0x50
	s_lshr_b32 s44, s8, 8
	s_lshl_b64 s[10:11], s[44:45], 21
	v_readlane_b32 s9, v251, 53
	s_waitcnt lgkmcnt(0)
	s_add_u32 s68, s6, s10
	s_addc_u32 s69, s7, s11
	s_lshl_b64 s[6:7], s[44:45], 20
	s_add_u32 s54, s9, s6
	v_readlane_b32 s6, v251, 54
	s_addc_u32 s55, s6, s7
	s_and_b32 s89, s8, 0xff
	s_mov_b64 s[6:7], 0

.LBB0_1224:
	v_mov_b32_e32 v0, v181
	v_readlane_b32 s8, v251, 6
	v_mbcnt_lo_u32_b32 v0, -1, v0
	v_mbcnt_hi_u32_b32 v203, -1, v0
	v_and_b32_e32 v205, 63, v203
	v_or_b32_e32 v0, s8, v205
	v_mul_hi_i32 v1, v0, s30
	v_lshrrev_b32_e32 v2, 31, v1
	v_ashrrev_i32_e32 v1, 2, v1
	v_add_u32_e32 v2, v1, v2
	v_mad_u64_u32 v[4:5], s[8:9], v2, s91, v[0:1]
	v_lshrrev_b32_e32 v1, 1, v2
	v_xor_b32_e32 v1, v1, v203
	v_bfi_b32 v1, -8, v4, v1
	v_cmp_lt_i32_e32 vcc, 15, v1
	v_ashrrev_i32_e32 v3, 31, v2
	v_lshlrev_b32_e32 v4, 3, v1
	s_and_saveexec_b64 s[8:9], vcc
	s_xor_b64 s[8:9], exec, s[8:9]
	v_lshlrev_b64 v[2:3], 7, v[2:3]
	v_lshl_add_u64 v[2:3], s[50:51], 0, v[2:3]
	v_add_u32_e32 v180, 0xffffff80, v4
	v_lshl_add_u64 v[16:17], v[180:181], 1, v[2:3]
	s_or_saveexec_b64 s[8:9], s[8:9]
	v_mov_b64_e32 v[18:19], 0x1000
	s_xor_b64 exec, exec, s[8:9]
	v_lshlrev_b64 v[2:3], 8, v[2:3]
	v_lshl_add_u64 v[2:3], s[48:49], 0, v[2:3]
	v_ashrrev_i32_e32 v5, 31, v4
	v_lshl_add_u64 v[16:17], v[4:5], 1, v[2:3]
	v_mov_b64_e32 v[18:19], 0x2000
	s_or_b64 exec, exec, s[8:9]
	v_add_u32_e32 v4, 0x200, v0
	v_mul_hi_i32 v1, v4, s30
	v_lshrrev_b32_e32 v2, 31, v1
	v_ashrrev_i32_e32 v1, 2, v1
	v_add_u32_e32 v2, v1, v2
	v_lshrrev_b32_e32 v1, 1, v2
	v_mad_u64_u32 v[4:5], s[8:9], v2, s91, v[4:5]
	v_xor_b32_e32 v1, v1, v203
	v_bfi_b32 v1, -8, v4, v1
	v_cmp_lt_i32_e32 vcc, 15, v1
	v_ashrrev_i32_e32 v3, 31, v2
	v_lshlrev_b32_e32 v4, 3, v1
	s_and_saveexec_b64 s[8:9], vcc
	s_xor_b64 s[8:9], exec, s[8:9]
	v_lshlrev_b64 v[2:3], 7, v[2:3]
	v_lshl_add_u64 v[2:3], s[50:51], 0, v[2:3]
	v_add_u32_e32 v180, 0xffffff80, v4
	v_lshl_add_u64 v[20:21], v[180:181], 1, v[2:3]
	s_or_saveexec_b64 s[8:9], s[8:9]
	v_mov_b64_e32 v[22:23], 0x1000
	s_xor_b64 exec, exec, s[8:9]
	v_lshlrev_b64 v[2:3], 8, v[2:3]
	v_lshl_add_u64 v[2:3], s[48:49], 0, v[2:3]
	v_ashrrev_i32_e32 v5, 31, v4
	v_lshl_add_u64 v[20:21], v[4:5], 1, v[2:3]
	v_mov_b64_e32 v[22:23], 0x2000
	s_or_b64 exec, exec, s[8:9]
	v_add_u32_e32 v2, 0x400, v0
	v_mul_hi_i32 v0, v2, s30
	v_lshrrev_b32_e32 v1, 31, v0
	v_ashrrev_i32_e32 v0, 2, v0
	v_add_u32_e32 v0, v0, v1
	v_lshrrev_b32_e32 v1, 1, v0
	v_mad_u64_u32 v[2:3], s[8:9], v0, s91, v[2:3]
	v_xor_b32_e32 v1, v1, v203
	v_bfi_b32 v2, -8, v2, v1
	v_cmp_lt_i32_e32 vcc, 15, v2
	v_ashrrev_i32_e32 v1, 31, v0
	v_lshlrev_b32_e32 v2, 3, v2
	s_and_saveexec_b64 s[8:9], vcc
	s_xor_b64 s[8:9], exec, s[8:9]
	v_lshlrev_b64 v[0:1], 7, v[0:1]
	v_lshl_add_u64 v[0:1], s[50:51], 0, v[0:1]
	v_add_u32_e32 v180, 0xffffff80, v2
	v_lshl_add_u64 v[24:25], v[180:181], 1, v[0:1]
	s_or_saveexec_b64 s[8:9], s[8:9]
	v_mov_b64_e32 v[26:27], 0x1000
	s_xor_b64 exec, exec, s[8:9]
	v_lshlrev_b64 v[0:1], 8, v[0:1]
	v_lshl_add_u64 v[0:1], s[48:49], 0, v[0:1]
	v_ashrrev_i32_e32 v3, 31, v2
	v_lshl_add_u64 v[24:25], v[2:3], 1, v[0:1]
	v_mov_b64_e32 v[26:27], 0x2000
	s_or_b64 exec, exec, s[8:9]
	s_xor_b64 s[58:59], s[4:5], -1
	s_xor_b64 s[60:61], s[6:7], -1
	s_and_b64 s[4:5], s[4:5], exec
	s_cselect_b32 s57, s79, s70
	s_lshl_b32 s21, s57, 8
	s_add_i32 s44, s21, s26
	s_add_u32 s66, s46, s44
	s_mov_b32 s4, s45
	s_mov_b32 s5, s45
	s_addc_u32 s67, s47, 0
	s_mov_b32 s6, s45
	s_mov_b32 s7, s45
	s_mov_b32 s8, s45
	s_mov_b32 s9, s45
	s_mov_b32 s10, s45
	s_mov_b32 s11, s45
	s_mov_b32 s12, s45
	s_mov_b32 s13, s45
	s_mov_b32 s14, s45
	s_mov_b32 s15, s45
	s_mov_b32 s16, s45
	s_mov_b32 s17, s45
	s_mov_b32 s18, s45
	s_mov_b32 s19, s45
	v_mov_b64_e32 v[0:1], s[4:5]
	v_mov_b64_e32 v[2:3], s[6:7]
	v_mov_b64_e32 v[4:5], s[8:9]
	v_mov_b64_e32 v[6:7], s[10:11]
	v_mov_b64_e32 v[8:9], s[12:13]
	v_mov_b64_e32 v[10:11], s[14:15]
	v_mov_b64_e32 v[12:13], s[16:17]
	v_mov_b64_e32 v[14:15], s[18:19]
	s_lshl_b64 s[4:5], s[66:67], 9
	v_readlane_b32 s6, v251, 38
	s_add_u32 s8, s6, s4
	v_readlane_b32 s4, v251, 39
	s_addc_u32 s9, s4, s5
	s_lshl_b64 s[4:5], s[66:67], 4
	v_readlane_b32 s6, v251, 43
	s_add_u32 s6, s6, s4
	v_readlane_b32 s4, v251, 45
	s_addc_u32 s7, s4, s5
	s_lshl_b64 s[4:5], s[44:45], 8
	v_readlane_b32 s10, v251, 47
	s_mov_b32 m0, s88
	s_add_u32 s4, s10, s4
	v_readlane_b32 s10, v251, 48
	s_addc_u32 s5, s10, s5
	global_load_lds_dwordx4 v[16:17], off
	v_lshlrev_b32_e32 v180, 1, v18
	s_add_i32 m0, s88, 0x2000
	v_lshrrev_b32_e32 v204, 5, v205
	v_readlane_b32 s10, v251, 63
	v_and_b32_e32 v200, 31, v203
	s_waitcnt vmcnt(0)
	v_lshl_add_u64 v[126:127], v[16:17], 0, v[180:181]
	global_load_lds_dwordx4 v[20:21], off
	s_mov_b32 m0, s86
	v_or_b32_e32 v16, s10, v204
	v_lshlrev_b32_e32 v184, 1, v22
	v_mov_b32_e32 v185, v181
	global_load_lds_dwordx4 v[24:25], off
	s_mov_b32 m0, s27
	v_bitop3_b32 v18, v16, v200, 9 bitop3:0x6c
	v_and_or_b32 v16, v16, 17, s96
	v_mov_b32_e32 v17, v181
	v_lshl_add_u64 v[188:189], v[20:21], 0, v[184:185]
	v_lshlrev_b32_e32 v186, 1, v26
	v_mov_b32_e32 v187, v181
	global_load_lds_dwordx4 v[126:127], off
	s_mov_b32 m0, s38
	v_lshlrev_b64 v[16:17], 9, v[16:17]
	v_lshl_add_u64 v[120:121], v[24:25], 0, v[186:187]
	global_load_lds_dwordx4 v[188:189], off
	s_mov_b32 m0, s39
	v_lshl_add_u64 v[16:17], s[34:35], 0, v[16:17]
	v_lshlrev_b32_e32 v18, 4, v18
	v_mov_b32_e32 v19, v181
	v_readlane_b32 s10, v250, 27
	global_load_lds_dwordx4 v[120:121], off
	v_lshl_add_u64 v[16:17], v[16:17], 0, v[18:19]
	s_mov_b32 m0, s10
	v_readlane_b32 s10, v251, 57
	global_load_lds_dwordx4 v[16:17], off
	s_nop 0
	v_or_b32_e32 v16, s10, v204
	v_bitop3_b32 v18, v16, v200, 11 bitop3:0x6c
	v_and_or_b32 v16, v16, 19, s96
	v_mov_b32_e32 v17, v181
	v_lshlrev_b64 v[16:17], 9, v[16:17]
	v_lshl_add_u64 v[16:17], s[34:35], 0, v[16:17]
	v_lshlrev_b32_e32 v18, 4, v18
	v_lshl_add_u64 v[16:17], v[16:17], 0, v[18:19]
	s_mov_b32 m0, s74
	v_readlane_b32 s10, v251, 61
	global_load_lds_dwordx4 v[16:17], off
	s_nop 0
	v_or_b32_e32 v16, s10, v204
	v_bitop3_b32 v18, v16, v200, 13 bitop3:0x6c
	v_and_or_b32 v16, v16, 17, s82
	v_mov_b32_e32 v17, v181
	v_lshlrev_b64 v[16:17], 9, v[16:17]
	v_lshl_add_u64 v[16:17], s[34:35], 0, v[16:17]
	v_lshlrev_b32_e32 v18, 4, v18
	v_lshl_add_u64 v[16:17], v[16:17], 0, v[18:19]
	s_mov_b32 m0, s76
	v_readlane_b32 s10, v250, 0
	global_load_lds_dwordx4 v[16:17], off
	s_nop 0
	v_or_b32_e32 v16, s10, v204
	v_bitop3_b32 v18, v16, v200, 15 bitop3:0x6c
	v_and_or_b32 v16, v16, 19, s82
	v_mov_b32_e32 v17, v181
	v_lshlrev_b64 v[16:17], 9, v[16:17]
	v_lshl_add_u64 v[16:17], s[34:35], 0, v[16:17]
	v_lshlrev_b32_e32 v18, 4, v18
	v_lshl_add_u64 v[16:17], v[16:17], 0, v[18:19]
	s_mov_b32 m0, s78
	v_readlane_b32 s10, v250, 6
	global_load_lds_dwordx4 v[16:17], off
	s_nop 0
	v_or_b32_e32 v16, s10, v204
	v_bitop3_b32 v18, v16, v200, 9 bitop3:0x6c
	v_and_or_b32 v16, v16, 17, s84
	v_mov_b32_e32 v17, v181
	v_lshlrev_b64 v[16:17], 9, v[16:17]
	v_lshl_add_u64 v[16:17], s[34:35], 0, v[16:17]
	v_lshlrev_b32_e32 v18, 4, v18
	v_lshl_add_u64 v[16:17], v[16:17], 0, v[18:19]
	s_mov_b32 m0, s94
	v_readlane_b32 s10, v250, 9
	global_load_lds_dwordx4 v[16:17], off
	s_nop 0
	v_or_b32_e32 v16, s10, v204
	v_bitop3_b32 v18, v16, v200, 11 bitop3:0x6c
	v_and_or_b32 v16, v16, 19, s36
	v_mov_b32_e32 v17, v181
	v_lshlrev_b64 v[16:17], 9, v[16:17]
	v_lshl_add_u64 v[16:17], s[34:35], 0, v[16:17]
	v_lshlrev_b32_e32 v18, 4, v18
	v_lshl_add_u64 v[16:17], v[16:17], 0, v[18:19]
	s_mov_b32 m0, s24
	v_lshlrev_b32_e32 v20, 9, v200
	global_load_lds_dwordx4 v[16:17], off
	v_or_b32_e32 v16, s73, v204
	v_bitop3_b32 v18, v16, v200, 13 bitop3:0x6c
	v_and_or_b32 v16, v16, 17, s37
	v_mov_b32_e32 v17, v181
	v_lshlrev_b64 v[16:17], 9, v[16:17]
	v_lshl_add_u64 v[16:17], s[34:35], 0, v[16:17]
	v_lshlrev_b32_e32 v18, 4, v18
	v_lshl_add_u64 v[16:17], v[16:17], 0, v[18:19]
	s_mov_b32 m0, s28
	v_mov_b32_e32 v21, v181
	global_load_lds_dwordx4 v[16:17], off
	v_or_b32_e32 v16, s72, v204
	v_bitop3_b32 v18, v16, v200, 15 bitop3:0x6c
	v_and_or_b32 v16, v16, 19, s85
	v_mov_b32_e32 v17, v181
	v_lshlrev_b64 v[16:17], 9, v[16:17]
	v_lshl_add_u64 v[16:17], s[34:35], 0, v[16:17]
	v_lshlrev_b32_e32 v18, 4, v18
	v_lshl_add_u64 v[16:17], v[16:17], 0, v[18:19]
	s_mov_b32 m0, s90
	v_lshlrev_b32_e32 v18, 8, v204
	global_load_lds_dwordx4 v[16:17], off
	v_or_b32_e32 v16, s97, v204
	v_bitop3_b32 v26, v16, v200, 9 bitop3:0x6c
	v_and_or_b32 v16, v16, 17, s83
	v_mov_b32_e32 v17, v181
	v_lshlrev_b64 v[22:23], 9, v[16:17]
	v_lshl_add_u64 v[16:17], s[8:9], 0, v[20:21]
	v_lshl_add_u64 v[24:25], v[16:17], 0, v[18:19]
	global_load_dwordx4 v[16:19], v[24:25], off
	global_load_dwordx4 v[172:175], v[24:25], off offset:16
	v_lshl_add_u64 v[22:23], s[34:35], 0, v[22:23]
	v_lshlrev_b32_e32 v26, 4, v26
	v_mov_b32_e32 v27, v181
	v_lshl_add_u64 v[22:23], v[22:23], 0, v[26:27]
	s_mov_b32 m0, s31
	v_or_b32_e32 v21, s41, v204
	global_load_lds_dwordx4 v[22:23], off
	v_and_or_b32 v22, v21, 19, s92
	v_mov_b32_e32 v23, v181
	v_bitop3_b32 v26, v21, v200, 11 bitop3:0x6c
	v_lshlrev_b64 v[22:23], 9, v[22:23]
	v_lshl_add_u64 v[22:23], s[34:35], 0, v[22:23]
	v_lshlrev_b32_e32 v26, 4, v26
	v_lshl_add_u64 v[22:23], v[22:23], 0, v[26:27]
	s_mov_b32 m0, s42
	v_or_b32_e32 v21, s75, v204
	global_load_lds_dwordx4 v[22:23], off
	v_and_or_b32 v22, v21, 17, s93
	v_mov_b32_e32 v23, v181
	v_bitop3_b32 v26, v21, v200, 13 bitop3:0x6c
	v_lshlrev_b64 v[22:23], 9, v[22:23]
	v_lshl_add_u64 v[22:23], s[34:35], 0, v[22:23]
	v_lshlrev_b32_e32 v26, 4, v26
	v_lshl_add_u64 v[22:23], v[22:23], 0, v[26:27]
	s_mov_b32 m0, s87
	v_or_b32_e32 v21, s77, v204
	global_load_lds_dwordx4 v[22:23], off
	v_and_or_b32 v22, v21, 19, s95
	v_mov_b32_e32 v23, v181
	v_bitop3_b32 v26, v21, v200, 15 bitop3:0x6c
	v_lshlrev_b64 v[22:23], 9, v[22:23]
	v_lshl_add_u64 v[22:23], s[34:35], 0, v[22:23]
	v_lshlrev_b32_e32 v26, 4, v26
	v_lshl_add_u64 v[22:23], v[22:23], 0, v[26:27]
	s_mov_b32 m0, s71
	v_lshlrev_b32_e32 v21, 4, v200
	global_load_lds_dwordx4 v[22:23], off
	global_load_dwordx4 v[168:171], v[24:25], off offset:32
	global_load_dwordx4 v[112:115], v[24:25], off offset:48
	global_load_dwordx4 v[116:119], v[24:25], off offset:64
	global_load_dwordx4 v[122:125], v[24:25], off offset:80
	global_load_dwordx4 v[164:167], v[24:25], off offset:96
	global_load_dwordx4 v[160:163], v[24:25], off offset:112
	global_load_dwordx4 v[156:159], v[24:25], off offset:128
	global_load_dwordx4 v[152:155], v[24:25], off offset:144
	global_load_dwordx4 v[148:151], v[24:25], off offset:160
	global_load_dwordx4 v[128:131], v[24:25], off offset:176
	global_load_dwordx4 v[144:147], v[24:25], off offset:192
	global_load_dwordx4 v[140:143], v[24:25], off offset:208
	global_load_dwordx4 v[132:135], v[24:25], off offset:224
	global_load_dwordx4 v[136:139], v[24:25], off offset:240
	v_lshlrev_b32_e32 v23, 4, v204
	v_and_b32_e32 v201, 15, v203
	global_load_dwordx4 v[176:179], v21, s[6:7]
	v_or_b32_e32 v21, v23, v201
	v_add_u32_e32 v22, 0, v20
	v_lshlrev_b32_e32 v21, 4, v21
	v_add_u32_e32 v24, v22, v21
	s_waitcnt vmcnt(0)
	s_waitcnt vmcnt(0) lgkmcnt(0)
	s_barrier
	ds_read_b128 v[24:27], v24 offset:49152
	v_add_u32_e32 v28, 0x10000, v22
	s_waitcnt lgkmcnt(0)
	v_mfma_f32_32x32x16_bf16 v[64:79], v[24:27], v[16:19], 0
	v_add_u32_e32 v24, v28, v21
	ds_read_b128 v[24:27], v24
	v_add_u32_e32 v221, s43, v20
	v_add_u32_e32 v218, 0x20400, v22
	v_readlane_b32 s6, v251, 6
	s_lshl_b32 s9, s57, 2
	s_add_i32 s9, s9, 4
	s_waitcnt lgkmcnt(0)
	v_mfma_f32_32x32x16_bf16 v[48:63], v[24:27], v[16:19], 0
	v_bitop3_b32 v24, v23, v201, 1 bitop3:0x36
	v_lshlrev_b32_e32 v202, 4, v24
	v_add_u32_e32 v24, v22, v202
	ds_read_b128 v[24:27], v24 offset:49152
	v_add_u32_e32 v222, v221, v202
	s_ashr_i32 s11, s89, 31
	s_mov_b32 s10, 3
	s_waitcnt lgkmcnt(0)
	v_mfma_f32_32x32x16_bf16 v[64:79], v[24:27], v[172:175], v[64:79]
	v_add_u32_e32 v24, v28, v202
	ds_read_b128 v[24:27], v24
	ds_read_b128 v[222:225], v222
	s_waitcnt lgkmcnt(1)
	v_mfma_f32_32x32x16_bf16 v[48:63], v[24:27], v[172:175], v[48:63]
	v_bitop3_b32 v24, v23, v201, 2 bitop3:0x36
	v_lshlrev_b32_e32 v220, 4, v24
	v_add_u32_e32 v24, v22, v220
	ds_read_b128 v[24:27], v24 offset:49152
	s_waitcnt lgkmcnt(0)
	v_mfma_f32_32x32x16_bf16 v[64:79], v[24:27], v[168:171], v[64:79]
	v_add_u32_e32 v24, v28, v220
	ds_read_b128 v[24:27], v24
	s_waitcnt lgkmcnt(0)
	v_mfma_f32_32x32x16_bf16 v[48:63], v[24:27], v[168:171], v[48:63]
	v_bitop3_b32 v24, v23, v201, 3 bitop3:0x36
	v_lshlrev_b32_e32 v219, 4, v24
	v_add_u32_e32 v24, v22, v219
	ds_read_b128 v[24:27], v24 offset:49152
	s_waitcnt lgkmcnt(0)
	v_mfma_f32_32x32x16_bf16 v[64:79], v[24:27], v[112:115], v[64:79]
	v_add_u32_e32 v24, v28, v219
	ds_read_b128 v[24:27], v24
	s_waitcnt lgkmcnt(0)
	v_mfma_f32_32x32x16_bf16 v[48:63], v[24:27], v[112:115], v[48:63]
	v_bitop3_b32 v24, v23, v201, 4 bitop3:0x36
	v_lshlrev_b32_e32 v217, 4, v24
	v_add_u32_e32 v24, v22, v217
	ds_read_b128 v[24:27], v24 offset:49152
	s_waitcnt lgkmcnt(0)
	v_mfma_f32_32x32x16_bf16 v[64:79], v[24:27], v[116:119], v[64:79]
	v_add_u32_e32 v24, v28, v217
	ds_read_b128 v[24:27], v24
	s_waitcnt lgkmcnt(0)
	v_mfma_f32_32x32x16_bf16 v[48:63], v[24:27], v[116:119], v[48:63]
	v_bitop3_b32 v24, v23, v201, 5 bitop3:0x36
	v_lshlrev_b32_e32 v216, 4, v24
	v_add_u32_e32 v24, v22, v216
	ds_read_b128 v[24:27], v24 offset:49152
	s_waitcnt lgkmcnt(0)
	v_mfma_f32_32x32x16_bf16 v[64:79], v[24:27], v[122:125], v[64:79]
	v_add_u32_e32 v24, v28, v216
	ds_read_b128 v[24:27], v24
	s_waitcnt lgkmcnt(0)
	v_mfma_f32_32x32x16_bf16 v[48:63], v[24:27], v[122:125], v[48:63]
	v_bitop3_b32 v24, v23, v201, 6 bitop3:0x36
	v_lshlrev_b32_e32 v215, 4, v24
	v_add_u32_e32 v24, v22, v215
	ds_read_b128 v[24:27], v24 offset:49152
	s_waitcnt lgkmcnt(0)
	v_mfma_f32_32x32x16_bf16 v[64:79], v[24:27], v[164:167], v[64:79]
	v_add_u32_e32 v24, v28, v215
	ds_read_b128 v[24:27], v24
	s_waitcnt lgkmcnt(0)
	v_mfma_f32_32x32x16_bf16 v[48:63], v[24:27], v[164:167], v[48:63]
	v_bitop3_b32 v24, v23, v201, 7 bitop3:0x36
	v_lshlrev_b32_e32 v214, 4, v24
	v_add_u32_e32 v24, v22, v214
	ds_read_b128 v[24:27], v24 offset:49152
	s_waitcnt lgkmcnt(0)
	v_mfma_f32_32x32x16_bf16 v[64:79], v[24:27], v[160:163], v[64:79]
	v_add_u32_e32 v24, v28, v214
	ds_read_b128 v[24:27], v24
	s_waitcnt lgkmcnt(0)
	v_mfma_f32_32x32x16_bf16 v[48:63], v[24:27], v[160:163], v[48:63]
	v_bitop3_b32 v24, v23, v201, 8 bitop3:0x36
	v_lshlrev_b32_e32 v210, 4, v24
	v_add_u32_e32 v24, v22, v210
	ds_read_b128 v[24:27], v24 offset:49152
	s_waitcnt lgkmcnt(0)
	v_mfma_f32_32x32x16_bf16 v[64:79], v[24:27], v[156:159], v[64:79]
	v_add_u32_e32 v24, v28, v210
	ds_read_b128 v[24:27], v24
	s_waitcnt lgkmcnt(0)
	v_mfma_f32_32x32x16_bf16 v[48:63], v[24:27], v[156:159], v[48:63]
	v_bitop3_b32 v24, v23, v201, 9 bitop3:0x36
	v_lshlrev_b32_e32 v211, 4, v24
	v_add_u32_e32 v24, v22, v211
	ds_read_b128 v[24:27], v24 offset:49152
	s_waitcnt lgkmcnt(0)
	v_mfma_f32_32x32x16_bf16 v[64:79], v[24:27], v[152:155], v[64:79]
	v_add_u32_e32 v24, v28, v211
	ds_read_b128 v[24:27], v24
	s_waitcnt lgkmcnt(0)
	v_mfma_f32_32x32x16_bf16 v[48:63], v[24:27], v[152:155], v[48:63]
	v_bitop3_b32 v24, v23, v201, 10 bitop3:0x36
	v_lshlrev_b32_e32 v212, 4, v24
	v_add_u32_e32 v24, v22, v212
	ds_read_b128 v[24:27], v24 offset:49152
	s_waitcnt lgkmcnt(0)
	v_mfma_f32_32x32x16_bf16 v[64:79], v[24:27], v[148:151], v[64:79]
	v_add_u32_e32 v24, v28, v212
	ds_read_b128 v[24:27], v24
	s_waitcnt lgkmcnt(0)
	v_mfma_f32_32x32x16_bf16 v[48:63], v[24:27], v[148:151], v[48:63]
	v_bitop3_b32 v24, v23, v201, 11 bitop3:0x36
	v_lshlrev_b32_e32 v213, 4, v24
	v_add_u32_e32 v24, v22, v213
	ds_read_b128 v[24:27], v24 offset:49152
	s_waitcnt lgkmcnt(0)
	v_mfma_f32_32x32x16_bf16 v[64:79], v[24:27], v[128:131], v[64:79]
	v_add_u32_e32 v24, v28, v213
	ds_read_b128 v[24:27], v24
	s_waitcnt lgkmcnt(0)
	v_mfma_f32_32x32x16_bf16 v[48:63], v[24:27], v[128:131], v[48:63]
	v_bitop3_b32 v24, v23, v201, 12 bitop3:0x36
	v_lshlrev_b32_e32 v206, 4, v24
	v_add_u32_e32 v24, v22, v206
	ds_read_b128 v[24:27], v24 offset:49152
	s_waitcnt lgkmcnt(0)
	v_mfma_f32_32x32x16_bf16 v[64:79], v[24:27], v[144:147], v[64:79]
	v_add_u32_e32 v24, v28, v206
	ds_read_b128 v[24:27], v24
	s_waitcnt lgkmcnt(0)
	v_mfma_f32_32x32x16_bf16 v[48:63], v[24:27], v[144:147], v[48:63]
	v_bitop3_b32 v24, v23, v201, 13 bitop3:0x36
	v_lshlrev_b32_e32 v207, 4, v24
	v_add_u32_e32 v24, v22, v207
	ds_read_b128 v[24:27], v24 offset:49152
	s_waitcnt lgkmcnt(0)
	v_mfma_f32_32x32x16_bf16 v[64:79], v[24:27], v[140:143], v[64:79]
	v_add_u32_e32 v24, v28, v207
	ds_read_b128 v[24:27], v24
	s_waitcnt lgkmcnt(0)
	v_mfma_f32_32x32x16_bf16 v[48:63], v[24:27], v[140:143], v[48:63]
	v_bitop3_b32 v24, v23, v201, 14 bitop3:0x36
	v_lshlrev_b32_e32 v208, 4, v24
	v_add_u32_e32 v24, v22, v208
	ds_read_b128 v[24:27], v24 offset:49152
	v_bitop3_b32 v23, v23, v203, 15 bitop3:0x72
	v_lshlrev_b32_e32 v209, 4, v23
	v_add_u32_e32 v23, v22, v209
	s_waitcnt lgkmcnt(0)
	v_mfma_f32_32x32x16_bf16 v[64:79], v[24:27], v[132:135], v[64:79]
	v_add_u32_e32 v24, v28, v208
	ds_read_b128 v[24:27], v24
	s_waitcnt lgkmcnt(0)
	v_mfma_f32_32x32x16_bf16 v[48:63], v[24:27], v[132:135], v[48:63]
	ds_read_b128 v[24:27], v23 offset:49152
	v_add_u32_e32 v23, v28, v209
	v_add_u32_e32 v28, 0x18000, v22
	v_add_u32_e32 v29, v28, v213
	s_waitcnt lgkmcnt(0)
	v_mfma_f32_32x32x16_bf16 v[64:79], v[24:27], v[136:139], v[64:79]
	ds_read_b128 v[24:27], v23
	v_add_u32_e32 v23, s33, v20
	v_add_u32_e32 v20, v221, v21
	s_waitcnt lgkmcnt(0)
	v_mfma_f32_32x32x16_bf16 v[48:63], v[24:27], v[136:139], v[48:63]
	v_add_u32_e32 v24, v23, v21
	ds_read_b128 v[24:27], v24
	s_waitcnt lgkmcnt(0)
	v_mfma_f32_32x32x16_bf16 v[96:111], v[24:27], v[16:19], 0
	v_add_u32_e32 v24, v28, v21
	ds_read_b128 v[24:27], v24
	s_waitcnt lgkmcnt(0)
	v_mfma_f32_32x32x16_bf16 v[80:95], v[24:27], v[16:19], 0
	v_add_u32_e32 v24, v23, v202
	ds_read_b128 v[24:27], v24
	s_waitcnt lgkmcnt(0)
	v_mfma_f32_32x32x16_bf16 v[96:111], v[24:27], v[172:175], v[96:111]
	v_add_u32_e32 v24, v28, v202
	ds_read_b128 v[24:27], v24
	v_add_u32_e32 v202, v218, v202
	s_waitcnt lgkmcnt(0)
	v_mfma_f32_32x32x16_bf16 v[80:95], v[24:27], v[172:175], v[80:95]
	v_add_u32_e32 v24, v23, v220
	ds_read_b128 v[24:27], v24
	s_waitcnt lgkmcnt(0)
	v_mfma_f32_32x32x16_bf16 v[96:111], v[24:27], v[168:171], v[96:111]
	v_add_u32_e32 v24, v28, v220
	ds_read_b128 v[24:27], v24
	s_waitcnt lgkmcnt(0)
	v_mfma_f32_32x32x16_bf16 v[80:95], v[24:27], v[168:171], v[80:95]
	v_add_u32_e32 v24, v23, v219
	ds_read_b128 v[24:27], v24
	s_waitcnt lgkmcnt(0)
	v_mfma_f32_32x32x16_bf16 v[96:111], v[24:27], v[112:115], v[96:111]
	v_add_u32_e32 v24, v28, v219
	ds_read_b128 v[24:27], v24
	s_waitcnt lgkmcnt(0)
	v_mfma_f32_32x32x16_bf16 v[80:95], v[24:27], v[112:115], v[80:95]
	v_add_u32_e32 v24, v23, v217
	ds_read_b128 v[24:27], v24
	s_waitcnt lgkmcnt(0)
	v_mfma_f32_32x32x16_bf16 v[96:111], v[24:27], v[116:119], v[96:111]
	v_add_u32_e32 v24, v28, v217
	ds_read_b128 v[24:27], v24
	s_waitcnt lgkmcnt(0)
	v_mfma_f32_32x32x16_bf16 v[80:95], v[24:27], v[116:119], v[80:95]
	v_add_u32_e32 v24, v23, v216
	ds_read_b128 v[24:27], v24
	s_waitcnt lgkmcnt(0)
	v_mfma_f32_32x32x16_bf16 v[96:111], v[24:27], v[122:125], v[96:111]
	v_add_u32_e32 v24, v28, v216
	ds_read_b128 v[24:27], v24
	s_waitcnt lgkmcnt(0)
	v_mfma_f32_32x32x16_bf16 v[80:95], v[24:27], v[122:125], v[80:95]
	v_add_u32_e32 v24, v23, v215
	ds_read_b128 v[24:27], v24
	s_waitcnt lgkmcnt(0)
	v_mfma_f32_32x32x16_bf16 v[96:111], v[24:27], v[164:167], v[96:111]
	v_add_u32_e32 v24, v28, v215
	ds_read_b128 v[24:27], v24
	s_waitcnt lgkmcnt(0)
	v_mfma_f32_32x32x16_bf16 v[80:95], v[24:27], v[164:167], v[80:95]
	v_add_u32_e32 v24, v23, v214
	ds_read_b128 v[24:27], v24
	s_waitcnt lgkmcnt(0)
	v_mfma_f32_32x32x16_bf16 v[96:111], v[24:27], v[160:163], v[96:111]
	v_add_u32_e32 v24, v28, v214
	ds_read_b128 v[24:27], v24
	s_waitcnt lgkmcnt(0)
	v_mfma_f32_32x32x16_bf16 v[80:95], v[24:27], v[160:163], v[80:95]
	v_add_u32_e32 v24, v23, v210
	ds_read_b128 v[24:27], v24
	s_waitcnt lgkmcnt(0)
	v_mfma_f32_32x32x16_bf16 v[96:111], v[24:27], v[156:159], v[96:111]
	v_add_u32_e32 v24, v28, v210
	ds_read_b128 v[24:27], v24
	s_waitcnt lgkmcnt(0)
	v_mfma_f32_32x32x16_bf16 v[80:95], v[24:27], v[156:159], v[80:95]
	v_add_u32_e32 v24, v23, v211
	ds_read_b128 v[24:27], v24
	s_waitcnt lgkmcnt(0)
	v_mfma_f32_32x32x16_bf16 v[96:111], v[24:27], v[152:155], v[96:111]
	v_add_u32_e32 v24, v28, v211
	ds_read_b128 v[24:27], v24
	s_waitcnt lgkmcnt(0)
	v_mfma_f32_32x32x16_bf16 v[80:95], v[24:27], v[152:155], v[80:95]
	v_add_u32_e32 v24, v23, v212
	ds_read_b128 v[24:27], v24
	s_waitcnt lgkmcnt(0)
	v_mfma_f32_32x32x16_bf16 v[96:111], v[24:27], v[148:151], v[96:111]
	v_add_u32_e32 v24, v28, v212
	ds_read_b128 v[24:27], v24
	s_waitcnt lgkmcnt(0)
	v_mfma_f32_32x32x16_bf16 v[80:95], v[24:27], v[148:151], v[80:95]
	v_add_u32_e32 v24, v23, v213
	ds_read_b128 v[24:27], v24
	s_waitcnt lgkmcnt(0)
	v_mfma_f32_32x32x16_bf16 v[96:111], v[24:27], v[128:131], v[96:111]
	ds_read_b128 v[24:27], v29
	v_add_u32_e32 v29, v23, v206
	s_waitcnt lgkmcnt(0)
	v_mfma_f32_32x32x16_bf16 v[80:95], v[24:27], v[128:131], v[80:95]
	ds_read_b128 v[24:27], v29
	v_add_u32_e32 v29, v28, v206
	s_waitcnt lgkmcnt(0)
	v_mfma_f32_32x32x16_bf16 v[96:111], v[24:27], v[144:147], v[96:111]
	ds_read_b128 v[24:27], v29
	v_add_u32_e32 v29, v23, v207
	s_waitcnt lgkmcnt(0)
	v_mfma_f32_32x32x16_bf16 v[80:95], v[24:27], v[144:147], v[80:95]
	ds_read_b128 v[24:27], v29
	v_add_u32_e32 v29, v28, v207
	s_waitcnt lgkmcnt(0)
	v_mfma_f32_32x32x16_bf16 v[96:111], v[24:27], v[140:143], v[96:111]
	ds_read_b128 v[24:27], v29
	v_add_u32_e32 v29, v23, v208
	v_add_u32_e32 v23, v23, v209
	s_waitcnt lgkmcnt(0)
	v_mfma_f32_32x32x16_bf16 v[80:95], v[24:27], v[140:143], v[80:95]
	ds_read_b128 v[24:27], v29
	v_add_u32_e32 v29, v28, v208
	s_waitcnt lgkmcnt(0)
	v_mfma_f32_32x32x16_bf16 v[96:111], v[24:27], v[132:135], v[96:111]
	ds_read_b128 v[24:27], v29
	s_waitcnt lgkmcnt(0)
	v_mfma_f32_32x32x16_bf16 v[80:95], v[24:27], v[132:135], v[80:95]
	ds_read_b128 v[24:27], v23
	v_add_u32_e32 v23, v28, v209
	s_waitcnt lgkmcnt(0)
	v_mfma_f32_32x32x16_bf16 v[96:111], v[24:27], v[136:139], v[96:111]
	ds_read_b128 v[24:27], v23
	s_waitcnt lgkmcnt(0)
	v_mfma_f32_32x32x16_bf16 v[80:95], v[24:27], v[136:139], v[80:95]
	ds_read_b128 v[24:27], v20
	v_add_u32_e32 v20, v218, v21
	ds_read_b128 v[20:23], v20
	s_waitcnt lgkmcnt(1)
	v_mfma_f32_32x32x16_bf16 v[32:47], v[24:27], v[16:19], 0
	v_mfma_f32_32x32x16_bf16 v[32:47], v[222:225], v[172:175], v[32:47]
	ds_read_b128 v[222:225], v202
	v_add_u32_e32 v202, v221, v220
	ds_read_b128 v[226:229], v202
	s_waitcnt lgkmcnt(2)
	v_mfma_f32_32x32x16_bf16 v[16:31], v[20:23], v[16:19], 0
	s_waitcnt lgkmcnt(1)
	v_mfma_f32_32x32x16_bf16 v[16:31], v[222:225], v[172:175], v[16:31]
	v_lshl_add_u64 v[174:175], v[126:127], 0, v[180:181]
	v_add_u32_e32 v126, v218, v220
	ds_read_b128 v[222:225], v126
	v_mov_b32_e32 v126, v177
	v_add_u32_e32 v177, v221, v219
	v_mov_b32_e32 v127, v178
	v_lshl_add_u64 v[172:173], v[188:189], 0, v[184:185]
	s_waitcnt lgkmcnt(1)
	v_mfma_f32_32x32x16_bf16 v[32:47], v[226:229], v[168:171], v[32:47]
	ds_read_b128 v[226:229], v177
	v_mov_b32_e32 v177, v179
	v_add_f32_e64 v126, v126, v176
	v_add_f32_e64 v127, v127, v177
	v_lshl_add_u64 v[188:189], v[120:121], 0, v[186:187]
	v_add_f32_e32 v126, v126, v127
	v_add_u32_e32 v127, v218, v219
	ds_read_b128 v[176:179], v127
	s_waitcnt lgkmcnt(2)
	v_mfma_f32_32x32x16_bf16 v[16:31], v[222:225], v[168:171], v[16:31]
	v_fmamk_f32 v126, v126, 0x3b800000, v198
	v_rsq_f32_e32 v126, v126
	v_lshlrev_b32_e32 v120, 8, v200
	v_mov_b32_e32 v121, v181
	v_lshl_add_u64 v[170:171], s[4:5], 0, v[120:121]
	v_mul_f32_e32 v168, 0x3dd53b94, v126
	v_lshlrev_b32_e32 v169, 3, v204
	v_add_u32_e32 v120, v221, v217
	ds_read_b128 v[222:225], v120
	v_pk_mul_f32 v[64:65], v[168:169], v[64:65] op_sel_hi:[0,1]
	s_waitcnt lgkmcnt(2)
	v_mfma_f32_32x32x16_bf16 v[32:47], v[226:229], v[112:115], v[32:47]
	v_mul_f32_e64 v66, v168, v66
	v_mul_f32_e64 v67, v168, v67
	v_mul_f32_e64 v68, v168, v68
	v_mul_f32_e64 v69, v168, v69
	v_mul_f32_e64 v70, v168, v70
	v_mul_f32_e64 v71, v168, v71
	v_pk_mul_f32 v[48:49], v[168:169], v[48:49] op_sel_hi:[0,1]
	v_cvt_pk_bf16_f32 v120, v48, v49
	v_add_u32_e32 v48, v221, v215
	v_pk_mul_f32 v[78:79], v[168:169], v[78:79] op_sel_hi:[0,1]
	s_waitcnt lgkmcnt(1)
	v_mfma_f32_32x32x16_bf16 v[16:31], v[176:179], v[112:115], v[16:31]
	v_cvt_pk_bf16_f32 v112, v64, v65
	v_add_u32_e32 v64, v218, v217
	v_cvt_pk_bf16_f32 v113, v66, v67
	ds_read_b128 v[64:67], v64
	v_cvt_pk_bf16_f32 v114, v68, v69
	v_add_u32_e32 v68, v221, v216
	v_cvt_pk_bf16_f32 v115, v70, v71
	ds_read_b128 v[68:71], v68
	s_waitcnt lgkmcnt(2)
	v_mfma_f32_32x32x16_bf16 v[32:47], v[222:225], v[116:119], v[32:47]
	v_mul_f32_e64 v52, v168, v52
	v_mul_f32_e64 v53, v168, v53
	v_mul_f32_e64 v54, v168, v54
	v_mul_f32_e64 v55, v168, v55
	v_mul_f32_e64 v72, v168, v72
	v_mul_f32_e64 v73, v168, v73
	v_pk_mul_f32 v[60:61], v[168:169], v[60:61] op_sel_hi:[0,1]
	v_pk_mul_f32 v[62:63], v[168:169], v[62:63] op_sel_hi:[0,1]
	v_cvt_pk_bf16_f32 v126, v60, v61
	v_cvt_pk_bf16_f32 v127, v62, v63
	s_waitcnt lgkmcnt(1)
	v_mfma_f32_32x32x16_bf16 v[16:31], v[64:67], v[116:119], v[16:31]
	v_mul_f32_e64 v64, v168, v74
	v_mul_f32_e64 v65, v168, v75
	v_cvt_pk_bf16_f32 v117, v64, v65
	v_add_u32_e32 v64, v218, v216
	ds_read_b128 v[64:67], v64
	v_cvt_pk_bf16_f32 v119, v78, v79
	v_pk_mul_f32 v[78:79], v[168:169], v[88:89] op_sel_hi:[0,1]
	v_cvt_pk_bf16_f32 v116, v72, v73
	s_waitcnt lgkmcnt(1)
	v_mfma_f32_32x32x16_bf16 v[32:47], v[68:71], v[122:125], v[32:47]
	v_mul_f32_e64 v68, v168, v50
	v_mul_f32_e64 v69, v168, v51
	ds_read_b128 v[48:51], v48
	v_mul_f32_e64 v70, v168, v86
	v_mul_f32_e64 v71, v168, v87
	v_add_u32_e32 v86, v218, v213
	ds_read_b128 v[86:89], v86
	v_pk_mul_f32 v[60:61], v[168:169], v[100:101] op_sel_hi:[0,1]
	v_pk_mul_f32 v[62:63], v[168:169], v[102:103] op_sel_hi:[0,1]
	s_waitcnt lgkmcnt(2)
	v_mfma_f32_32x32x16_bf16 v[16:31], v[64:67], v[122:125], v[16:31]
	v_cvt_pk_bf16_f32 v122, v52, v53
	v_add_u32_e32 v52, v218, v215
	v_cvt_pk_bf16_f32 v123, v54, v55
	ds_read_b128 v[52:55], v52
	v_mul_f32_e64 v64, v168, v98
	v_mul_f32_e64 v65, v168, v99
	v_cvt_pk_bf16_f32 v98, v60, v61
	v_cvt_pk_bf16_f32 v99, v62, v63
	s_waitcnt lgkmcnt(2)
	v_mfma_f32_32x32x16_bf16 v[32:47], v[48:51], v[164:167], v[32:47]
	v_mul_f32_e64 v48, v168, v56
	v_mul_f32_e64 v49, v168, v57
	v_mul_f32_e64 v50, v168, v58
	v_mul_f32_e64 v51, v168, v59
	v_cvt_pk_bf16_f32 v124, v48, v49
	v_add_u32_e32 v48, v221, v214
	v_cvt_pk_bf16_f32 v125, v50, v51
	ds_read_b128 v[48:51], v48
	v_and_b32_e32 v58, 32, v205
	s_waitcnt lgkmcnt(1)
	v_mfma_f32_32x32x16_bf16 v[16:31], v[52:55], v[164:167], v[16:31]
	v_add_u32_e32 v52, v218, v214
	ds_read_b128 v[52:55], v52
	v_mov_b32_e32 v59, v181
	v_lshl_add_u64 v[72:73], v[170:171], 0, v[58:59]
	v_mul_f32_e64 v56, v168, v96
	v_mul_f32_e64 v57, v168, v97
	v_cvt_pk_bf16_f32 v96, v56, v57
	v_add_u32_e32 v56, v221, v210
	s_waitcnt lgkmcnt(1)
	v_mfma_f32_32x32x16_bf16 v[32:47], v[48:51], v[160:163], v[32:47]
	global_load_dwordx4 v[48:51], v[72:73], off offset:16
	ds_read_b128 v[56:59], v56
	v_cvt_pk_bf16_f32 v97, v64, v65
	v_mul_f32_e64 v64, v168, v106
	v_mul_f32_e64 v65, v168, v107
	v_cvt_pk_bf16_f32 v101, v64, v65
	v_cvt_pk_bf16_f32 v121, v68, v69
	v_pk_mul_f32 v[68:69], v[168:169], v[108:109] op_sel_hi:[0,1]
	s_waitcnt lgkmcnt(1)
	v_mfma_f32_32x32x16_bf16 v[16:31], v[52:55], v[160:163], v[16:31]
	v_add_u32_e32 v52, v221, v211
	ds_read_b128 v[60:63], v52
	global_load_dwordx4 v[52:55], v[72:73], off
	v_cvt_pk_bf16_f32 v102, v68, v69
	v_mul_f32_e64 v68, v168, v84
	v_mul_f32_e64 v69, v168, v85
	v_cvt_pk_bf16_f32 v106, v68, v69
	v_add_u32_e32 v68, v221, v207
	s_waitcnt lgkmcnt(1)
	v_mfma_f32_32x32x16_bf16 v[32:47], v[56:59], v[156:159], v[32:47]
	v_mul_f32_e64 v58, v168, v104
	v_mul_f32_e64 v59, v168, v105
	v_cvt_pk_bf16_f32 v100, v58, v59
	v_add_u32_e32 v58, v221, v212
	ds_read_b128 v[64:67], v58
	v_pk_mul_f32 v[56:57], v[168:169], v[110:111] op_sel_hi:[0,1]
	v_cvt_pk_bf16_f32 v103, v56, v57
	v_add_u32_e32 v56, v221, v213
	s_waitcnt lgkmcnt(1)
	v_mfma_f32_32x32x16_bf16 v[32:47], v[60:63], v[152:155], v[32:47]
	ds_read_b128 v[60:63], v56
	v_cvt_pk_bf16_f32 v107, v70, v71
	ds_read_b128 v[68:71], v68
	v_mul_f32_e64 v76, v168, v76
	v_mul_f32_e64 v77, v168, v77
	v_cvt_pk_bf16_f32 v118, v76, v77
	v_pk_mul_f32 v[74:75], v[168:169], v[92:93] op_sel_hi:[0,1]
	v_pk_mul_f32 v[76:77], v[168:169], v[94:95] op_sel_hi:[0,1]
	s_waitcnt lgkmcnt(2)
	v_mfma_f32_32x32x16_bf16 v[32:47], v[64:67], v[148:151], v[32:47]
	v_mul_f32_e64 v64, v168, v80
	v_mul_f32_e64 v65, v168, v81
	v_mul_f32_e64 v66, v168, v82
	v_mul_f32_e64 v67, v168, v83
	v_cvt_pk_bf16_f32 v104, v64, v65
	v_add_u32_e32 v64, v221, v206
	v_cvt_pk_bf16_f32 v105, v66, v67
	ds_read_b128 v[64:67], v64
	global_load_dwordx4 v[56:59], v[72:73], off offset:80
	s_waitcnt lgkmcnt(2)
	v_mfma_f32_32x32x16_bf16 v[32:47], v[60:63], v[128:131], v[32:47]
	v_cvt_pk_bf16_f32 v110, v74, v75
	v_cvt_pk_bf16_f32 v111, v76, v77
	v_cvt_pk_bf16_f32 v108, v78, v79
	global_load_dwordx4 v[60:63], v[72:73], off offset:64
	global_load_dwordx4 v[164:167], v[72:73], off offset:128
	v_add_u32_e32 v94, v218, v207
	s_movk_i32 s4, 0x180
	s_waitcnt lgkmcnt(0)
	v_mfma_f32_32x32x16_bf16 v[32:47], v[64:67], v[144:147], v[32:47]
	v_mul_f32_e64 v64, v168, v90
	v_mul_f32_e64 v65, v168, v91
	v_cvt_pk_bf16_f32 v109, v64, v65
	v_add_u32_e32 v64, v221, v208
	ds_read_b128 v[64:67], v64
	v_add_u32_e32 v90, v218, v206
	ds_read_b128 v[90:93], v90
	v_or_b32_e32 v202, s6, v203
	v_mfma_f32_32x32x16_bf16 v[32:47], v[68:71], v[140:143], v[32:47]
	v_add_u32_e32 v68, v218, v210
	ds_read_b128 v[74:77], v68
	v_add_u32_e32 v68, v218, v211
	v_add_u32_e32 v69, v221, v209
	ds_read_b128 v[78:81], v68
	ds_read_b128 v[82:85], v69
	v_add_u32_e32 v68, v218, v212
	s_waitcnt lgkmcnt(4)
	v_mfma_f32_32x32x16_bf16 v[32:47], v[64:67], v[132:135], v[32:47]
	global_load_dwordx4 v[64:67], v[72:73], off offset:144
	ds_read_b128 v[68:71], v68
	s_sub_i32 s5, 0, s25
	s_waitcnt lgkmcnt(1)
	v_mfma_f32_32x32x16_bf16 v[32:47], v[82:85], v[136:139], v[32:47]
	ds_read_b128 v[82:85], v94
	v_add_u32_e32 v94, v218, v208
	ds_read_b128 v[160:163], v94
	v_add_u32_e32 v94, v218, v209
	ds_read_b128 v[176:179], v94
	s_nop 6
	v_mul_f32_e32 v36, v168, v36
	v_mfma_f32_32x32x16_bf16 v[16:31], v[74:77], v[156:159], v[16:31]
	v_mul_f32_e32 v74, v168, v37
	s_waitcnt vmcnt(5)
	v_pk_mul_f32 v[74:75], v[74:75], v[48:49] op_sel:[0,1] op_sel_hi:[0,0]
	v_pk_fma_f32 v[76:77], v[36:37], v[48:49], v[74:75] neg_lo:[0,0,1] neg_hi:[0,0,1]
	v_pk_fma_f32 v[48:49], v[36:37], v[48:49], v[74:75] op_sel_hi:[0,1,1]
	v_mul_f32_e32 v36, v168, v39
	v_mul_f32_e32 v48, v168, v38
	v_pk_mul_f32 v[74:75], v[36:37], v[50:51] op_sel:[0,1] op_sel_hi:[0,0]
	global_load_dwordx4 v[36:39], v[72:73], off offset:208
	v_mfma_f32_32x32x16_bf16 v[16:31], v[78:81], v[152:155], v[16:31]
	v_fma_f32 v78, v48, v50, -v74
	v_fma_f32 v79, v49, v51, -v75
	v_fma_f32 v50, v48, v50, v74
	v_fma_f32 v51, v48, v51, v75
	v_mul_f32_e32 v48, v168, v33
	v_mul_f32_e32 v32, v168, v32
	s_waitcnt vmcnt(5)
	v_pk_mul_f32 v[74:75], v[48:49], v[52:53] op_sel:[0,1] op_sel_hi:[0,0]
	v_pk_fma_f32 v[80:81], v[32:33], v[52:53], v[74:75] neg_lo:[0,0,1] neg_hi:[0,0,1]
	v_pk_fma_f32 v[52:53], v[32:33], v[52:53], v[74:75] op_sel_hi:[0,1,1]
	v_mul_f32_e32 v48, v168, v34
	v_mul_f32_e32 v50, v168, v35
	global_load_dwordx4 v[32:35], v[72:73], off offset:192
	s_waitcnt lgkmcnt(3)
	v_mfma_f32_32x32x16_bf16 v[16:31], v[68:71], v[148:151], v[16:31]
	v_mul_f32_e64 v68, v50, v55
	v_mul_f32_e64 v69, v50, v54
	v_fma_f32 v70, v48, v54, -v68
	v_fma_f32 v71, v49, v55, -v69
	v_fma_f32 v54, v48, v54, v68
	v_fma_f32 v55, v48, v55, v69
	v_mul_f32_e32 v48, v168, v45
	v_mul_f32_e32 v44, v168, v44
	v_mul_f32_e32 v40, v168, v40
	v_mov_b32_e32 v158, 0
	v_mfma_f32_32x32x16_bf16 v[16:31], v[86:89], v[128:131], v[16:31]
	v_cvt_pk_bf16_f32 v130, v76, v49
	v_cvt_pk_bf16_f32 v131, v78, v51
	v_cvt_pk_bf16_f32 v128, v80, v53
	v_cvt_pk_bf16_f32 v129, v70, v55
	s_cmp_eq_u32 s99, 0
	s_cselect_b32 s101, 1, 0
	s_cselect_b32 s99, 0, 2
	v_mov_b32_e32 v157, 0xf149f2ca
	s_cbranch_scc0 .Linit_done
	v_mov_b32_e32 v157, 0
.Linit_done:
	s_waitcnt lgkmcnt(0)
	s_barrier
	v_mfma_f32_32x32x16_bf16 v[16:31], v[90:93], v[144:147], v[16:31]
	v_lshlrev_b32_e32 v145, 2, v204
	s_waitcnt vmcnt(5)
	v_pk_mul_f32 v[48:49], v[48:49], v[56:57] op_sel:[0,1] op_sel_hi:[0,0]
	v_pk_fma_f32 v[50:51], v[44:45], v[56:57], v[48:49] neg_lo:[0,0,1] neg_hi:[0,0,1]
	v_pk_fma_f32 v[44:45], v[44:45], v[56:57], v[48:49] op_sel_hi:[0,1,1]
	v_mul_f32_e32 v44, v168, v46
	v_mul_f32_e32 v46, v168, v47
	v_pk_mul_f32 v[46:47], v[46:47], v[58:59] op_sel:[0,1] op_sel_hi:[0,0]
	v_mfma_f32_32x32x16_bf16 v[16:31], v[82:85], v[140:143], v[16:31]
	v_fma_f32 v48, v44, v58, -v46
	v_fma_f32 v49, v45, v59, -v47
	v_fma_f32 v46, v44, v58, v46
	v_fma_f32 v47, v44, v59, v47
	v_mul_f32_e32 v44, v168, v41
	s_waitcnt vmcnt(4)
	v_pk_mul_f32 v[52:53], v[44:45], v[60:61] op_sel:[0,1] op_sel_hi:[0,0]
	v_pk_fma_f32 v[54:55], v[40:41], v[60:61], v[52:53] neg_lo:[0,0,1] neg_hi:[0,0,1]
	v_pk_fma_f32 v[40:41], v[40:41], v[60:61], v[52:53] op_sel_hi:[0,1,1]
	v_mul_f32_e32 v40, v168, v42
	v_mfma_f32_32x32x16_bf16 v[16:31], v[160:163], v[132:135], v[16:31]
	v_mul_f32_e32 v42, v168, v43
	v_pk_mul_f32 v[42:43], v[42:43], v[62:63] op_sel:[0,1] op_sel_hi:[0,0]
	v_pk_fma_f32 v[52:53], v[40:41], v[62:63], v[42:43] neg_lo:[0,0,1] neg_hi:[0,0,1]
	v_pk_fma_f32 v[42:43], v[40:41], v[62:63], v[42:43] op_sel_hi:[0,1,1]
	v_cvt_pk_bf16_f32 v132, v54, v41
	v_cvt_pk_bf16_f32 v133, v52, v43
	v_cvt_pk_bf16_f32 v134, v50, v45
	v_mfma_f32_32x32x16_bf16 v[16:31], v[176:179], v[136:139], v[16:31]
	v_cvt_pk_bf16_f32 v135, v48, v47
	v_mov_b64_e32 v[62:63], v[14:15]
	v_mov_b64_e32 v[60:61], v[12:13]
	v_mov_b64_e32 v[58:59], v[10:11]
	v_mov_b64_e32 v[56:57], v[8:9]
	v_mov_b64_e32 v[54:55], v[6:7]
	v_mov_b64_e32 v[52:53], v[4:5]
	s_nop 4
	v_mul_f32_e32 v40, v168, v21
	v_mul_f32_e32 v20, v168, v20
	s_waitcnt vmcnt(2)
	v_pk_mul_f32 v[40:41], v[40:41], v[64:65] op_sel:[0,1] op_sel_hi:[0,0]
	v_pk_fma_f32 v[42:43], v[20:21], v[64:65], v[40:41] neg_lo:[0,0,1] neg_hi:[0,0,1]
	v_pk_fma_f32 v[20:21], v[20:21], v[64:65], v[40:41] op_sel_hi:[0,1,1]
	v_mul_f32_e32 v20, v168, v22
	v_mul_f32_e32 v22, v168, v23
	v_pk_mul_f32 v[22:23], v[22:23], v[66:67] op_sel:[0,1] op_sel_hi:[0,0]
	v_pk_fma_f32 v[40:41], v[20:21], v[66:67], v[22:23] neg_lo:[0,0,1] neg_hi:[0,0,1]
	v_pk_fma_f32 v[22:23], v[20:21], v[66:67], v[22:23] op_sel_hi:[0,1,1]
	v_mul_f32_e32 v20, v168, v17
	v_mul_f32_e32 v16, v168, v16
	v_pk_mul_f32 v[44:45], v[20:21], v[164:165] op_sel:[0,1] op_sel_hi:[0,0]
	v_pk_fma_f32 v[46:47], v[16:17], v[164:165], v[44:45] neg_lo:[0,0,1] neg_hi:[0,0,1]
	v_pk_fma_f32 v[16:17], v[16:17], v[164:165], v[44:45] op_sel_hi:[0,1,1]
	v_mul_f32_e32 v16, v168, v18
	v_mul_f32_e32 v18, v168, v19
	v_pk_mul_f32 v[18:19], v[18:19], v[166:167] op_sel:[0,1] op_sel_hi:[0,0]
	v_pk_fma_f32 v[44:45], v[16:17], v[166:167], v[18:19] neg_lo:[0,0,1] neg_hi:[0,0,1]
	v_pk_fma_f32 v[18:19], v[16:17], v[166:167], v[18:19] op_sel_hi:[0,1,1]
	v_mul_f32_e32 v18, v168, v29
	v_cvt_pk_bf16_f32 v137, v44, v19
	v_mul_f32_e32 v16, v168, v28
	s_waitcnt vmcnt(1)
	v_pk_mul_f32 v[18:19], v[18:19], v[36:37] op_sel:[0,1] op_sel_hi:[0,0]
	v_cvt_pk_bf16_f32 v136, v46, v17
	v_cvt_pk_bf16_f32 v138, v42, v21
	v_pk_fma_f32 v[20:21], v[16:17], v[36:37], v[18:19] neg_lo:[0,0,1] neg_hi:[0,0,1]
	v_pk_fma_f32 v[16:17], v[16:17], v[36:37], v[18:19] op_sel_hi:[0,1,1]
	v_mul_f32_e32 v18, v168, v31
	v_mul_f32_e32 v16, v168, v30
	v_pk_mul_f32 v[18:19], v[18:19], v[38:39] op_sel:[0,1] op_sel_hi:[0,0]
	v_cvt_pk_bf16_f32 v139, v40, v23
	v_pk_fma_f32 v[22:23], v[16:17], v[38:39], v[18:19] neg_lo:[0,0,1] neg_hi:[0,0,1]
	v_pk_fma_f32 v[18:19], v[16:17], v[38:39], v[18:19] op_sel_hi:[0,1,1]
	v_mul_f32_e32 v18, v168, v25
	v_mul_f32_e32 v16, v168, v24
	s_waitcnt vmcnt(0)
	v_pk_mul_f32 v[24:25], v[18:19], v[32:33] op_sel:[0,1] op_sel_hi:[0,0]
	v_mul_f32_e32 v18, v168, v27
	v_pk_fma_f32 v[28:29], v[16:17], v[32:33], v[24:25] neg_lo:[0,0,1] neg_hi:[0,0,1]
	v_pk_fma_f32 v[24:25], v[16:17], v[32:33], v[24:25] op_sel_hi:[0,1,1]
	v_mul_f32_e32 v16, v168, v26
	v_pk_mul_f32 v[26:27], v[18:19], v[34:35] op_sel:[0,1] op_sel_hi:[0,0]
	v_pk_fma_f32 v[30:31], v[16:17], v[34:35], v[26:27] neg_lo:[0,0,1] neg_hi:[0,0,1]
	v_pk_fma_f32 v[26:27], v[16:17], v[34:35], v[26:27] op_sel_hi:[0,1,1]
	v_cvt_pk_bf16_f32 v142, v20, v17
	v_lshrrev_b32_e32 v17, 1, v203
	v_mad_u32_u24 v16, v200, s4, 0
	v_bfe_u32 v18, v203, 1, 3
	v_bitop3_b32 v17, v204, v17, 7 bitop3:0x78
	v_lshl_add_u32 v147, v17, 4, v16
	v_bitop3_b32 v17, v204, v18, 2 bitop3:0x36
	v_lshl_add_u32 v148, v17, 4, v16
	v_bitop3_b32 v17, v204, v18, 4 bitop3:0x36
	v_lshl_add_u32 v149, v17, 4, v16
	v_bitop3_b32 v17, v204, v18, 6 bitop3:0x36
	v_lshl_add_u32 v150, v17, 4, v16
	v_lshrrev_b32_e32 v16, 3, v202
	v_bfe_u32 v17, v202, 3, 1
	v_and_b32_e32 v16, 2, v16
	v_bfe_u32 v18, v203, 1, 1
	v_bfe_u32 v20, v203, 2, 1
	v_lshlrev_b32_e32 v21, 3, v17
	v_cvt_pk_bf16_f32 v143, v22, v19
	v_or_b32_e32 v19, v16, v18
	v_or3_b32 v20, v21, v20, v145
	v_lshlrev_b32_e32 v21, 1, v204
	v_bitop3_b32 v16, v16, v21, v18 bitop3:0x36
	v_bitop3_b32 v18, v21, v19, 1 bitop3:0x36
	v_cvt_f32_ubyte0_e32 v21, s25
	v_lshlrev_b32_e32 v22, 3, v203
	v_lshlrev_b32_e32 v17, 6, v17
	v_lshlrev_b32_e32 v18, 4, v18
	v_rcp_iflag_f32_e32 v21, v21
	v_and_b32_e32 v22, 8, v22
	v_mad_u32_u24 v20, v20, s4, 0
	v_or_b32_e32 v19, v18, v17
	v_lshl_add_u32 v16, v16, 4, v20
	v_add3_u32 v152, v20, v19, v22
	v_xor_b32_e32 v19, 64, v17
	v_add3_u32 v151, v16, v17, v22
	v_add3_u32 v153, v16, v19, v22
	v_bitop3_b32 v16, v18, v17, 64 bitop3:0xf6
	v_add3_u32 v154, v20, v16, v22
	v_mul_f32_e32 v16, 0x4f7ffffe, v21
	v_cvt_u32_f32_e32 v16, v16
	s_abs_i32 s4, s89
	v_cvt_pk_bf16_f32 v140, v28, v25
	v_cvt_pk_bf16_f32 v141, v30, v27
	v_readfirstlane_b32 s6, v16
	s_mul_i32 s5, s5, s6
	s_mul_hi_u32 s5, s6, s5
	s_add_i32 s6, s6, s5
	s_mul_hi_u32 s5, s4, s6
	s_mul_i32 s6, s5, s25
	s_sub_i32 s4, s4, s6
	s_add_i32 s6, s5, 1
	s_sub_i32 s7, s4, s25
	s_cmp_ge_u32 s4, s25
	s_cselect_b32 s5, s6, s5
	s_cselect_b32 s4, s7, s4
	s_add_i32 s6, s5, 1
	s_cmp_ge_u32 s4, s25
	s_cselect_b32 s4, s6, s5
	s_xor_b32 s12, s4, s11
	s_sub_i32 s8, s12, s11
	s_mul_i32 s4, s8, s25
	s_sub_i32 s4, s89, s4
	s_lshl_b32 s6, s4, 5
	s_ashr_i32 s7, s6, 31
	s_lshl_b64 s[4:5], s[6:7], 2
	s_add_u32 s4, s68, s4
	s_addc_u32 s5, s69, s5
	v_lshl_or_b32 v16, s12, 6, v196
	s_lshl_b32 s7, s11, 6
	v_subrev_u32_e32 v155, s7, v16
	s_add_i32 s7, s29, s21
	v_add_u32_e32 v16, s7, v200
	v_sub_u32_e32 v156, v16, v145
	v_mov_b64_e32 v[46:47], v[14:15]
	v_mov_b64_e32 v[30:31], v[14:15]
	s_movk_i32 s7, 0x7f
	s_mov_b32 s11, 3
	s_mov_b32 s12, s40
	v_mov_b64_e32 v[44:45], v[12:13]
	v_mov_b64_e32 v[42:43], v[10:11]
	v_mov_b64_e32 v[40:41], v[8:9]
	v_mov_b64_e32 v[38:39], v[6:7]
	v_mov_b64_e32 v[36:37], v[4:5]
	v_mov_b64_e32 v[34:35], v[2:3]
	v_mov_b64_e32 v[32:33], v[0:1]
	v_mov_b64_e32 v[50:51], v[2:3]
	v_mov_b64_e32 v[48:49], v[0:1]
	v_mov_b64_e32 v[28:29], v[12:13]
	v_mov_b64_e32 v[26:27], v[10:11]
	v_mov_b64_e32 v[24:25], v[8:9]
	v_mov_b64_e32 v[22:23], v[6:7]
	v_mov_b64_e32 v[20:21], v[4:5]
	v_mov_b64_e32 v[18:19], v[2:3]
	v_mov_b64_e32 v[16:17], v[0:1]
	s_branch .LBB0_1238

.LBB0_1244:
	s_cmp_lg_u32 s101, 0
	s_cbranch_scc1 .Lf_a
	s_nop 7
	v_max3_f32 v144, v80, v81, v82
	v_max3_f32 v144, v144, v83, v84
	v_max3_f32 v146, v64, v65, v66
	v_max3_f32 v144, v144, v85, v86
	v_max3_f32 v146, v146, v67, v68
	v_max3_f32 v144, v144, v87, v88
	v_max3_f32 v146, v146, v69, v70
	v_max3_f32 v144, v144, v89, v90
	v_max3_f32 v146, v146, v71, v72
	v_max3_f32 v144, v144, v91, v92
	v_max3_f32 v146, v146, v73, v74
	v_max3_f32 v144, v144, v93, v94
	v_max3_f32 v146, v146, v75, v76
	v_max3_f32 v146, v146, v77, v78
	v_max3_f32 v144, v144, v95, v79
	v_max_f32_e32 v144, v144, v146
	v_mov_b32_e32 v146, v144
	s_nop 1
	v_permlane32_swap_b32_e32 v144, v146
	v_max_f32_e32 v146, v146, v146
	v_max_f32_e32 v144, v144, v144
	v_max_f32_e32 v146, v144, v146
	v_sub_f32_e32 v144, v146, v157
	v_cmp_ge_f32_e32 vcc, s0, v144
	s_cmp_eq_u64 vcc, exec
	v_mov_b32_e32 v144, 1.0
	s_cbranch_scc1 .LBB0_1246
	v_max_f32_e32 v144, v146, v146
	v_max_f32_e32 v146, v157, v157
	v_max_f32_e32 v146, v146, v144
	v_sub_f32_e32 v144, v157, v146
	v_exp_f32_e32 v144, v144
	v_mov_b32_e32 v157, v146
	v_pk_mul_f32 v[62:63], v[62:63], v[144:145] op_sel_hi:[1,0]
	v_pk_mul_f32 v[60:61], v[60:61], v[144:145] op_sel_hi:[1,0]
	v_pk_mul_f32 v[58:59], v[58:59], v[144:145] op_sel_hi:[1,0]
	v_pk_mul_f32 v[56:57], v[56:57], v[144:145] op_sel_hi:[1,0]
	v_pk_mul_f32 v[54:55], v[54:55], v[144:145] op_sel_hi:[1,0]
	v_pk_mul_f32 v[52:53], v[52:53], v[144:145] op_sel_hi:[1,0]
	v_pk_mul_f32 v[50:51], v[50:51], v[144:145] op_sel_hi:[1,0]
	v_pk_mul_f32 v[48:49], v[48:49], v[144:145] op_sel_hi:[1,0]
	v_pk_mul_f32 v[46:47], v[46:47], v[144:145] op_sel_hi:[1,0]
	v_pk_mul_f32 v[44:45], v[44:45], v[144:145] op_sel_hi:[1,0]
	v_pk_mul_f32 v[42:43], v[42:43], v[144:145] op_sel_hi:[1,0]
	v_pk_mul_f32 v[40:41], v[40:41], v[144:145] op_sel_hi:[1,0]
	v_pk_mul_f32 v[38:39], v[38:39], v[144:145] op_sel_hi:[1,0]
	v_pk_mul_f32 v[36:37], v[36:37], v[144:145] op_sel_hi:[1,0]
	v_pk_mul_f32 v[34:35], v[34:35], v[144:145] op_sel_hi:[1,0]
	v_pk_mul_f32 v[32:33], v[32:33], v[144:145] op_sel_hi:[1,0]
	v_pk_mul_f32 v[14:15], v[14:15], v[144:145] op_sel_hi:[1,0]
	v_pk_mul_f32 v[12:13], v[12:13], v[144:145] op_sel_hi:[1,0]
	v_pk_mul_f32 v[10:11], v[10:11], v[144:145] op_sel_hi:[1,0]
	v_pk_mul_f32 v[8:9], v[8:9], v[144:145] op_sel_hi:[1,0]
	v_pk_mul_f32 v[6:7], v[6:7], v[144:145] op_sel_hi:[1,0]
	v_pk_mul_f32 v[4:5], v[4:5], v[144:145] op_sel_hi:[1,0]
	v_pk_mul_f32 v[2:3], v[2:3], v[144:145] op_sel_hi:[1,0]
	v_pk_mul_f32 v[0:1], v[0:1], v[144:145] op_sel_hi:[1,0]
	v_pk_mul_f32 v[30:31], v[30:31], v[144:145] op_sel_hi:[1,0]
	v_pk_mul_f32 v[28:29], v[28:29], v[144:145] op_sel_hi:[1,0]
	v_pk_mul_f32 v[26:27], v[26:27], v[144:145] op_sel_hi:[1,0]
	v_pk_mul_f32 v[24:25], v[24:25], v[144:145] op_sel_hi:[1,0]
	v_pk_mul_f32 v[22:23], v[22:23], v[144:145] op_sel_hi:[1,0]
	v_pk_mul_f32 v[20:21], v[20:21], v[144:145] op_sel_hi:[1,0]
	v_pk_mul_f32 v[18:19], v[18:19], v[144:145] op_sel_hi:[1,0]
	v_pk_mul_f32 v[16:17], v[16:17], v[144:145] op_sel_hi:[1,0]

.Lf_a:
	s_nop 7
	v_mov_b32_e32 v144, 1.0
	v_exp_f32_e32 v80, v80
	v_exp_f32_e32 v81, v81
	v_exp_f32_e32 v82, v82
	v_exp_f32_e32 v83, v83
	v_add_f32_e32 v146, 0, v80
	v_exp_f32_e32 v84, v84
	v_add_f32_e32 v146, v81, v146
	v_exp_f32_e32 v85, v85
	v_add_f32_e32 v146, v82, v146
	v_exp_f32_e32 v86, v86
	v_add_f32_e32 v146, v83, v146
	v_exp_f32_e32 v87, v87
	v_add_f32_e32 v146, v84, v146
	v_exp_f32_e32 v88, v88
	v_add_f32_e32 v146, v85, v146
	v_exp_f32_e32 v89, v89
	v_add_f32_e32 v146, v86, v146
	v_exp_f32_e32 v90, v90
	v_add_f32_e32 v146, v87, v146
	v_exp_f32_e32 v91, v91
	v_add_f32_e32 v146, v88, v146
	v_exp_f32_e32 v92, v92
	v_add_f32_e32 v146, v89, v146
	v_exp_f32_e32 v93, v93
	v_add_f32_e32 v146, v90, v146
	v_exp_f32_e32 v94, v94
	v_add_f32_e32 v146, v91, v146
	v_exp_f32_e32 v95, v95
	v_add_f32_e32 v146, v92, v146
	v_exp_f32_e32 v64, v64
	v_add_f32_e32 v146, v93, v146
	v_exp_f32_e32 v65, v65
	v_add_f32_e32 v146, v94, v146
	v_exp_f32_e32 v66, v66
	v_add_f32_e32 v146, v95, v146
	v_exp_f32_e32 v67, v67
	v_add_f32_e32 v146, v64, v146
	v_exp_f32_e32 v68, v68
	v_add_f32_e32 v146, v65, v146
	v_exp_f32_e32 v69, v69
	v_add_f32_e32 v146, v66, v146
	v_exp_f32_e32 v70, v70
	v_add_f32_e32 v146, v67, v146
	v_exp_f32_e32 v71, v71
	v_add_f32_e32 v146, v68, v146
	v_exp_f32_e32 v161, v72
	v_add_f32_e32 v146, v69, v146
	v_add_f32_e32 v146, v70, v146
	v_add_f32_e32 v146, v71, v146
	v_add_f32_e32 v72, v161, v146
	v_exp_f32_e32 v146, v73
	v_exp_f32_e32 v162, v74
	v_exp_f32_e32 v163, v75
	v_exp_f32_e32 v164, v76
	v_add_f32_e32 v72, v146, v72
	v_exp_f32_e32 v165, v77
	v_add_f32_e32 v72, v162, v72
	v_exp_f32_e32 v166, v78
	v_add_f32_e32 v72, v163, v72
	v_exp_f32_e32 v167, v79
	v_add_f32_e32 v72, v164, v72
	v_add_f32_e32 v72, v165, v72
	v_add_f32_e32 v72, v166, v72
	v_cvt_pk_bf16_f32 v76, v80, v81
	v_cvt_pk_bf16_f32 v77, v84, v85
	v_cvt_pk_bf16_f32 v78, v82, v83
	v_cvt_pk_bf16_f32 v79, v86, v87
	v_cvt_pk_bf16_f32 v64, v64, v65
	v_cvt_pk_bf16_f32 v65, v68, v69
	v_cvt_pk_bf16_f32 v68, v161, v146
	v_add_u32_e32 v146, s14, v151
	v_add_f32_e32 v159, v167, v72
	v_cvt_pk_bf16_f32 v72, v88, v89
	v_cvt_pk_bf16_f32 v73, v92, v93
	v_cvt_pk_bf16_f32 v74, v90, v91
	v_cvt_pk_bf16_f32 v75, v94, v95
	v_add_u32_e32 v161, s14, v152
	ds_read_b64_tr_b16 v[80:81], v146
	ds_read_b64_tr_b16 v[82:83], v161 offset:768
	ds_read_b64_tr_b16 v[84:85], v146 offset:6144
	ds_read_b64_tr_b16 v[86:87], v161 offset:6912
	ds_read_b64_tr_b16 v[88:89], v146 offset:12288
	ds_read_b64_tr_b16 v[90:91], v161 offset:13056
	ds_read_b64_tr_b16 v[92:93], v146 offset:18432
	ds_read_b64_tr_b16 v[94:95], v161 offset:19200
	s_waitcnt lgkmcnt(6)
	v_mfma_f32_32x32x16_bf16 v[48:63], v[80:83], v[76:79], v[48:63]
	v_cvt_pk_bf16_f32 v66, v66, v67
	v_cvt_pk_bf16_f32 v67, v70, v71
	v_cvt_pk_bf16_f32 v71, v166, v167
	v_add_u32_e32 v166, s14, v153
	v_cvt_pk_bf16_f32 v69, v164, v165
	v_cvt_pk_bf16_f32 v70, v162, v163
	v_add_u32_e32 v167, s14, v154
	ds_read_b64_tr_b16 v[162:163], v166
	ds_read_b64_tr_b16 v[164:165], v167 offset:768
	ds_read_b64_tr_b16 v[176:177], v166 offset:6144
	ds_read_b64_tr_b16 v[178:179], v167 offset:6912
	ds_read_b64_tr_b16 v[204:205], v166 offset:12288
	ds_read_b64_tr_b16 v[206:207], v167 offset:13056
	ds_read_b64_tr_b16 v[208:209], v166 offset:18432
	ds_read_b64_tr_b16 v[210:211], v167 offset:19200
	s_waitcnt lgkmcnt(12)
	v_mfma_f32_32x32x16_bf16 v[48:63], v[84:87], v[72:75], v[48:63]
	s_add_i32 s14, s10, -2
	s_and_b32 s14, s14, 3
	s_mulk_i32 s14, 0x6000
	v_mov_b32_e32 v160, v159
	s_nop 1
	v_permlane32_swap_b32_e32 v159, v160
	s_waitcnt lgkmcnt(6)
	v_mfma_f32_32x32x16_bf16 v[32:47], v[162:165], v[76:79], v[32:47]
	v_mfma_f32_32x32x16_bf16 v[48:63], v[88:91], v[64:67], v[48:63]
	s_waitcnt lgkmcnt(4)
	v_mfma_f32_32x32x16_bf16 v[32:47], v[176:179], v[72:75], v[32:47]
	v_mfma_f32_32x32x16_bf16 v[48:63], v[92:95], v[68:71], v[48:63]
	ds_read_b64_tr_b16 v[80:81], v146 offset:128
	ds_read_b64_tr_b16 v[82:83], v161 offset:896
	ds_read_b64_tr_b16 v[92:93], v146 offset:6272
	ds_read_b64_tr_b16 v[94:95], v161 offset:7040
	ds_read_b64_tr_b16 v[212:213], v146 offset:12416
	ds_read_b64_tr_b16 v[214:215], v161 offset:13184
	ds_read_b64_tr_b16 v[88:89], v146 offset:18560
	ds_read_b64_tr_b16 v[90:91], v161 offset:19328
	v_add_u32_e32 v146, s14, v147
	v_add_u32_e32 v161, s14, v148
	s_waitcnt lgkmcnt(10)
	v_mfma_f32_32x32x16_bf16 v[32:47], v[204:207], v[64:67], v[32:47]
	ds_read_b64_tr_b16 v[84:85], v166 offset:128
	ds_read_b64_tr_b16 v[86:87], v167 offset:896
	ds_read_b64_tr_b16 v[162:163], v166 offset:6272
	ds_read_b64_tr_b16 v[164:165], v167 offset:7040
	ds_read_b64_tr_b16 v[176:177], v166 offset:12416
	ds_read_b64_tr_b16 v[178:179], v167 offset:13184
	ds_read_b64_tr_b16 v[204:205], v166 offset:18560
	ds_read_b64_tr_b16 v[206:207], v167 offset:19328
	v_add_u32_e32 v166, s14, v149
	v_add_u32_e32 v167, s14, v150
	s_waitcnt lgkmcnt(14)
	v_mfma_f32_32x32x16_bf16 v[0:15], v[80:83], v[76:79], v[0:15]
	s_waitcnt lgkmcnt(6)
	v_mfma_f32_32x32x16_bf16 v[16:31], v[84:87], v[76:79], v[16:31]
	v_mfma_f32_32x32x16_bf16 v[0:15], v[92:95], v[72:75], v[0:15]
	s_waitcnt lgkmcnt(4)
	v_mfma_f32_32x32x16_bf16 v[16:31], v[162:165], v[72:75], v[16:31]
	v_mfma_f32_32x32x16_bf16 v[0:15], v[212:215], v[64:67], v[0:15]
	s_waitcnt lgkmcnt(2)
	v_mfma_f32_32x32x16_bf16 v[16:31], v[176:179], v[64:67], v[16:31]
	v_mfma_f32_32x32x16_bf16 v[32:47], v[208:211], v[68:71], v[32:47]
	v_mfma_f32_32x32x16_bf16 v[0:15], v[88:91], v[68:71], v[0:15]
	s_waitcnt lgkmcnt(0)
	v_mfma_f32_32x32x16_bf16 v[16:31], v[204:207], v[68:71], v[16:31]
	ds_read_b128 v[64:67], v146
	ds_read_b128 v[68:71], v146 offset:12288
	ds_read_b128 v[162:165], v161
	ds_read_b128 v[176:179], v161 offset:12288
	ds_read_b128 v[204:207], v166
	ds_read_b128 v[208:211], v166 offset:12288
	ds_read_b128 v[212:215], v167
	ds_read_b128 v[216:219], v167 offset:12288
	s_waitcnt lgkmcnt(7)
	v_mfma_f32_32x32x16_bf16 v[80:95], v[64:67], v[112:115], 0
	s_waitcnt lgkmcnt(6)
	v_mfma_f32_32x32x16_bf16 v[64:79], v[68:71], v[112:115], 0
	s_waitcnt lgkmcnt(5)
	v_mfma_f32_32x32x16_bf16 v[80:95], v[162:165], v[116:119], v[80:95]
	ds_read_b128 v[162:165], v146 offset:128
	ds_read_b128 v[220:223], v146 offset:12416
	s_waitcnt lgkmcnt(6)
	v_mfma_f32_32x32x16_bf16 v[64:79], v[176:179], v[116:119], v[64:79]
	s_waitcnt lgkmcnt(5)
	v_mfma_f32_32x32x16_bf16 v[80:95], v[204:207], v[120:123], v[80:95]
	ds_read_b128 v[176:179], v161 offset:128
	ds_read_b128 v[204:207], v161 offset:12416
	s_waitcnt lgkmcnt(6)
	v_mfma_f32_32x32x16_bf16 v[64:79], v[208:211], v[120:123], v[64:79]
	s_waitcnt lgkmcnt(5)
	v_mfma_f32_32x32x16_bf16 v[80:95], v[212:215], v[124:127], v[80:95]
	ds_read_b128 v[208:211], v166 offset:128
	ds_read_b128 v[212:215], v166 offset:12416
	s_waitcnt lgkmcnt(6)
	v_mfma_f32_32x32x16_bf16 v[64:79], v[216:219], v[124:127], v[64:79]
	s_waitcnt lgkmcnt(5)
	v_mfma_f32_32x32x16_bf16 v[80:95], v[162:165], v[96:99], v[80:95]
	ds_read_b128 v[162:165], v167 offset:128
	ds_read_b128 v[216:219], v167 offset:12416
	s_waitcnt lgkmcnt(6)
	v_mfma_f32_32x32x16_bf16 v[64:79], v[220:223], v[96:99], v[64:79]
	s_waitcnt lgkmcnt(5)
	v_mfma_f32_32x32x16_bf16 v[80:95], v[176:179], v[100:103], v[80:95]
	ds_read_b128 v[176:179], v146 offset:256
	ds_read_b128 v[220:223], v146 offset:12544
	s_waitcnt lgkmcnt(6)
	v_mfma_f32_32x32x16_bf16 v[64:79], v[204:207], v[100:103], v[64:79]
	s_waitcnt lgkmcnt(5)
	v_mfma_f32_32x32x16_bf16 v[80:95], v[208:211], v[104:107], v[80:95]
	ds_read_b128 v[204:207], v161 offset:256
	ds_read_b128 v[208:211], v161 offset:12544
	s_waitcnt lgkmcnt(6)
	v_mfma_f32_32x32x16_bf16 v[64:79], v[212:215], v[104:107], v[64:79]
	s_waitcnt lgkmcnt(5)
	v_mfma_f32_32x32x16_bf16 v[80:95], v[162:165], v[108:111], v[80:95]
	ds_read_b128 v[162:165], v166 offset:256
	ds_read_b128 v[212:215], v166 offset:12544
	s_waitcnt lgkmcnt(6)
	v_mfma_f32_32x32x16_bf16 v[64:79], v[216:219], v[108:111], v[64:79]
	s_waitcnt lgkmcnt(5)
	v_mfma_f32_32x32x16_bf16 v[80:95], v[176:179], v[128:131], v[80:95]
	ds_read_b128 v[176:179], v167 offset:256
	ds_read_b128 v[216:219], v167 offset:12544
	s_waitcnt lgkmcnt(6)
	v_mfma_f32_32x32x16_bf16 v[64:79], v[220:223], v[128:131], v[64:79]
	s_waitcnt lgkmcnt(5)
	v_mfma_f32_32x32x16_bf16 v[80:95], v[204:207], v[132:135], v[80:95]
	s_waitcnt lgkmcnt(4)
	v_mfma_f32_32x32x16_bf16 v[64:79], v[208:211], v[132:135], v[64:79]
	s_waitcnt lgkmcnt(3)
	v_mfma_f32_32x32x16_bf16 v[80:95], v[162:165], v[136:139], v[80:95]
	s_waitcnt lgkmcnt(2)
	v_mfma_f32_32x32x16_bf16 v[64:79], v[212:215], v[136:139], v[64:79]
	s_waitcnt lgkmcnt(1)
	v_mfma_f32_32x32x16_bf16 v[80:95], v[176:179], v[140:143], v[80:95]
	s_waitcnt lgkmcnt(0)
	v_mfma_f32_32x32x16_bf16 v[64:79], v[216:219], v[140:143], v[64:79]
	s_cmp_le_u32 s7, s44
	s_cbranch_scc1 .Lf_b
	v_add_u32_e32 v146, 59, v156
	v_cmp_gt_u32_e32 vcc, 2.0, v146
	v_add_u32_e32 v146, 27, v156
	s_nop 4
	v_cndmask_b32_e32 v80, v199, v80, vcc
	v_cmp_gt_u32_e32 vcc, 2.0, v146
	v_add_u32_e32 v146, 58, v156
	s_nop 0
	v_cndmask_b32_e32 v64, v199, v64, vcc
	v_cmp_gt_u32_e32 vcc, 2.0, v146
	v_add_u32_e32 v146, 26, v156
	s_nop 0
	v_cndmask_b32_e32 v81, v199, v81, vcc
	v_cmp_gt_u32_e32 vcc, 2.0, v146
	v_add_u32_e32 v146, 57, v156
	s_nop 0
	v_cndmask_b32_e32 v65, v199, v65, vcc
	v_cmp_gt_u32_e32 vcc, 2.0, v146
	v_add_u32_e32 v146, 25, v156
	s_nop 0
	v_cndmask_b32_e32 v82, v199, v82, vcc
	v_cmp_gt_u32_e32 vcc, 2.0, v146
	v_add_u32_e32 v146, 56, v156
	s_nop 0
	v_cndmask_b32_e32 v66, v199, v66, vcc
	v_cmp_gt_u32_e32 vcc, 2.0, v146
	v_add_u32_e32 v146, 24, v156
	s_nop 0
	v_cndmask_b32_e32 v83, v199, v83, vcc
	v_cmp_gt_u32_e32 vcc, 2.0, v146
	v_add_u32_e32 v146, 51, v156
	s_nop 0
	v_cndmask_b32_e32 v67, v199, v67, vcc
	v_cmp_gt_u32_e32 vcc, 2.0, v146
	v_add_u32_e32 v146, 19, v156
	s_nop 0
	v_cndmask_b32_e32 v84, v199, v84, vcc
	v_cmp_gt_u32_e32 vcc, 2.0, v146
	v_add_u32_e32 v146, 50, v156
	s_nop 0
	v_cndmask_b32_e32 v68, v199, v68, vcc
	v_cmp_gt_u32_e32 vcc, 2.0, v146
	v_add_u32_e32 v146, 18, v156
	s_nop 0
	v_cndmask_b32_e32 v85, v199, v85, vcc
	v_cmp_gt_u32_e32 vcc, 2.0, v146
	v_add_u32_e32 v146, 49, v156
	s_nop 0
	v_cndmask_b32_e32 v69, v199, v69, vcc
	v_cmp_gt_u32_e32 vcc, 2.0, v146
	v_add_u32_e32 v146, 17, v156
	s_nop 0
	v_cndmask_b32_e32 v86, v199, v86, vcc
	v_cmp_gt_u32_e32 vcc, 2.0, v146
	v_add_u32_e32 v146, 48, v156
	s_nop 0
	v_cndmask_b32_e32 v70, v199, v70, vcc
	v_cmp_gt_u32_e32 vcc, 2.0, v146
	v_add_u32_e32 v146, 16, v156
	s_nop 0
	v_cndmask_b32_e32 v87, v199, v87, vcc
	v_cmp_gt_u32_e32 vcc, 2.0, v146
	v_add_u32_e32 v146, 43, v156
	s_nop 0
	v_cndmask_b32_e32 v71, v199, v71, vcc
	v_cmp_gt_u32_e32 vcc, 2.0, v146
	v_add_u32_e32 v146, 11, v156
	s_nop 0
	v_cndmask_b32_e32 v88, v199, v88, vcc
	v_cmp_gt_u32_e32 vcc, 2.0, v146
	v_add_u32_e32 v146, 42, v156
	s_nop 0
	v_cndmask_b32_e32 v72, v199, v72, vcc
	v_cmp_gt_u32_e32 vcc, 2.0, v146
	v_add_u32_e32 v146, 10, v156
	s_nop 0
	v_cndmask_b32_e32 v89, v199, v89, vcc
	v_cmp_gt_u32_e32 vcc, 2.0, v146
	v_add_u32_e32 v146, 41, v156
	s_nop 0
	v_cndmask_b32_e32 v73, v199, v73, vcc
	v_cmp_gt_u32_e32 vcc, 2.0, v146
	v_add_u32_e32 v146, 9, v156
	s_nop 0
	v_cndmask_b32_e32 v90, v199, v90, vcc
	v_cmp_gt_u32_e32 vcc, 2.0, v146
	v_add_u32_e32 v146, 40, v156
	s_nop 0
	v_cndmask_b32_e32 v74, v199, v74, vcc
	v_cmp_gt_u32_e32 vcc, 2.0, v146
	v_add_u32_e32 v146, 8, v156
	s_nop 0
	v_cndmask_b32_e32 v91, v199, v91, vcc
	v_cmp_gt_u32_e32 vcc, 2.0, v146
	v_add_u32_e32 v146, 35, v156
	s_nop 0
	v_cndmask_b32_e32 v75, v199, v75, vcc
	v_cmp_gt_u32_e32 vcc, 2.0, v146
	v_add_u32_e32 v146, 3, v156
	s_nop 0
	v_cndmask_b32_e32 v92, v199, v92, vcc
	v_cmp_gt_u32_e32 vcc, 2.0, v146
	v_add_u32_e32 v146, 34, v156
	s_nop 0
	v_cndmask_b32_e32 v76, v199, v76, vcc
	v_cmp_gt_u32_e32 vcc, 2.0, v146
	v_add_u32_e32 v146, 2, v156
	s_nop 0
	v_cndmask_b32_e32 v93, v199, v93, vcc
	v_cmp_gt_u32_e32 vcc, 2.0, v146
	v_add_u32_e32 v146, 33, v156
	s_nop 0
	v_cndmask_b32_e32 v77, v199, v77, vcc
	v_cmp_gt_u32_e32 vcc, 2.0, v146
	v_add_u32_e32 v146, 1, v156
	s_nop 0
	v_cndmask_b32_e32 v94, v199, v94, vcc
	v_cmp_gt_u32_e32 vcc, 2.0, v146
	v_add_u32_e32 v146, 32, v156
	s_nop 0
	v_cndmask_b32_e32 v78, v199, v78, vcc
	v_cmp_gt_u32_e32 vcc, 2.0, v146
	s_nop 1
	v_cndmask_b32_e32 v95, v199, v95, vcc
	v_cmp_gt_u32_e32 vcc, 2.0, v156
	s_nop 1
	v_cndmask_b32_e32 v79, v199, v79, vcc
.Lf_b:
	s_nop 9
	v_mov_b32_e32 v146, 1.0
	v_exp_f32_e32 v170, v64
	v_exp_f32_e32 v171, v65
	v_exp_f32_e32 v176, v66
	v_exp_f32_e32 v177, v67
	v_exp_f32_e32 v178, v68
	v_exp_f32_e32 v179, v69
	v_exp_f32_e32 v161, v80
	v_exp_f32_e32 v185, v70
	v_exp_f32_e32 v162, v81
	v_exp_f32_e32 v187, v71
	v_exp_f32_e32 v163, v82
	v_exp_f32_e32 v203, v72
	v_exp_f32_e32 v164, v83
	v_exp_f32_e32 v204, v73
	v_exp_f32_e32 v165, v84
	v_exp_f32_e32 v205, v74
	v_exp_f32_e32 v166, v85
	v_exp_f32_e32 v206, v75
	v_exp_f32_e32 v167, v86
	v_exp_f32_e32 v207, v76
	v_add_u32_e32 v209, s14, v151
	v_exp_f32_e32 v168, v87
	v_exp_f32_e32 v208, v77
	v_add_u32_e32 v210, s14, v152
	ds_read_b64_tr_b16 v[64:65], v209
	ds_read_b64_tr_b16 v[66:67], v210 offset:768
	v_exp_f32_e32 v88, v88
	v_exp_f32_e32 v89, v89
	v_exp_f32_e32 v90, v90
	v_exp_f32_e32 v91, v91
	v_cvt_pk_bf16_f32 v72, v161, v162
	v_cvt_pk_bf16_f32 v73, v165, v166
	v_cvt_pk_bf16_f32 v74, v163, v164
	v_cvt_pk_bf16_f32 v75, v167, v168
	v_exp_f32_e32 v92, v92
	s_waitcnt lgkmcnt(0)
	v_mfma_f32_32x32x16_bf16 v[48:63], v[64:67], v[72:75], v[48:63]
	v_exp_f32_e32 v93, v93
	v_exp_f32_e32 v94, v94
	v_exp_f32_e32 v95, v95
	v_exp_f32_e32 v211, v78
	ds_read_b64_tr_b16 v[68:69], v209 offset:6144
	ds_read_b64_tr_b16 v[70:71], v210 offset:6912
	v_mov_b32_e32 v80, v79
	v_cvt_pk_bf16_f32 v76, v88, v89
	v_cvt_pk_bf16_f32 v77, v92, v93
	v_cvt_pk_bf16_f32 v78, v90, v91
	v_cvt_pk_bf16_f32 v79, v94, v95
	ds_read_b64_tr_b16 v[64:65], v209 offset:12288
	ds_read_b64_tr_b16 v[66:67], v210 offset:13056
	s_waitcnt lgkmcnt(2)
	v_mfma_f32_32x32x16_bf16 v[48:63], v[68:71], v[76:79], v[48:63]
	v_cvt_pk_bf16_f32 v68, v170, v171
	v_cvt_pk_bf16_f32 v69, v178, v179
	v_cvt_pk_bf16_f32 v70, v176, v177
	v_cvt_pk_bf16_f32 v71, v185, v187
	v_add_u32_e32 v213, s14, v153
	v_exp_f32_e32 v212, v80
	ds_read_b64_tr_b16 v[80:81], v209 offset:18432
	ds_read_b64_tr_b16 v[82:83], v210 offset:19200
	s_waitcnt lgkmcnt(2)
	v_mfma_f32_32x32x16_bf16 v[48:63], v[64:67], v[68:71], v[48:63]
	ds_read_b64_tr_b16 v[84:85], v213
	v_cvt_pk_bf16_f32 v64, v203, v204
	v_cvt_pk_bf16_f32 v65, v207, v208
	v_cvt_pk_bf16_f32 v66, v205, v206
	v_cvt_pk_bf16_f32 v67, v211, v212
	v_add_u32_e32 v214, s14, v154
	v_add_f32_e32 v159, v159, v160
	s_waitcnt lgkmcnt(1)
	v_mfma_f32_32x32x16_bf16 v[48:63], v[80:83], v[64:67], v[48:63]
	ds_read_b64_tr_b16 v[86:87], v214 offset:768
	ds_read_b64_tr_b16 v[80:81], v213 offset:6144
	v_fmac_f32_e32 v159, v158, v144
	s_addk_i32 s12, 0x1000
	s_add_i32 s11, s11, 4
	s_add_i32 s10, s10, 2
	s_addk_i32 s7, 0x80
	v_add_u32_e32 v155, 32, v155
	s_waitcnt lgkmcnt(1)
	v_mfma_f32_32x32x16_bf16 v[32:47], v[84:87], v[72:75], v[32:47]
	ds_read_b64_tr_b16 v[82:83], v214 offset:6912
	ds_read_b64_tr_b16 v[84:85], v213 offset:12288
	s_cmp_ge_u32 s13, s9
	v_add_u32_e32 v156, 0xffffff80, v156
	s_waitcnt lgkmcnt(1)
	v_mfma_f32_32x32x16_bf16 v[32:47], v[80:83], v[76:79], v[32:47]
	ds_read_b64_tr_b16 v[86:87], v214 offset:13056
	ds_read_b64_tr_b16 v[80:81], v213 offset:18432
	s_waitcnt lgkmcnt(1)
	v_mfma_f32_32x32x16_bf16 v[32:47], v[84:87], v[68:71], v[32:47]
	ds_read_b64_tr_b16 v[82:83], v214 offset:19200
	ds_read_b64_tr_b16 v[84:85], v209 offset:128
	ds_read_b64_tr_b16 v[86:87], v210 offset:896
	s_waitcnt lgkmcnt(0)
	v_mfma_f32_32x32x16_bf16 v[0:15], v[84:87], v[72:75], v[0:15]
	v_add_f32_e32 v84, 0, v161
	v_add_f32_e32 v84, v162, v84
	v_add_f32_e32 v84, v163, v84
	v_add_f32_e32 v84, v164, v84
	v_add_f32_e32 v144, v165, v84
	v_mfma_f32_32x32x16_bf16 v[32:47], v[80:83], v[64:67], v[32:47]
	ds_read_b64_tr_b16 v[80:81], v209 offset:6272
	ds_read_b64_tr_b16 v[82:83], v210 offset:7040
	ds_read_b64_tr_b16 v[84:85], v209 offset:12416
	ds_read_b64_tr_b16 v[86:87], v210 offset:13184
	s_waitcnt lgkmcnt(2)
	v_mfma_f32_32x32x16_bf16 v[0:15], v[80:83], v[76:79], v[0:15]
	v_add_f32_e32 v80, v166, v144
	v_add_f32_e32 v80, v167, v80
	v_add_f32_e32 v80, v168, v80
	v_add_f32_e32 v80, v88, v80
	v_add_f32_e32 v88, v89, v80
	ds_read_b64_tr_b16 v[80:81], v209 offset:18560
	ds_read_b64_tr_b16 v[82:83], v210 offset:19328
	s_waitcnt lgkmcnt(2)
	v_mfma_f32_32x32x16_bf16 v[0:15], v[84:87], v[68:71], v[0:15]
	v_add_f32_e32 v84, v90, v88
	v_add_f32_e32 v84, v91, v84
	v_add_f32_e32 v84, v92, v84
	v_add_f32_e32 v84, v93, v84
	v_add_f32_e32 v88, v94, v84
	ds_read_b64_tr_b16 v[84:85], v213 offset:128
	ds_read_b64_tr_b16 v[86:87], v214 offset:896
	s_waitcnt lgkmcnt(2)
	v_mfma_f32_32x32x16_bf16 v[0:15], v[80:83], v[64:67], v[0:15]
	v_add_f32_e32 v80, v95, v88
	v_add_f32_e32 v80, v170, v80
	v_add_f32_e32 v80, v171, v80
	v_add_f32_e32 v80, v176, v80
	v_add_f32_e32 v88, v177, v80
	ds_read_b64_tr_b16 v[80:81], v213 offset:6272
	ds_read_b64_tr_b16 v[82:83], v214 offset:7040
	s_waitcnt lgkmcnt(2)
	v_mfma_f32_32x32x16_bf16 v[16:31], v[84:87], v[72:75], v[16:31]
	v_add_f32_e32 v72, v178, v88
	v_add_f32_e32 v72, v179, v72
	v_add_f32_e32 v72, v185, v72
	v_add_f32_e32 v72, v187, v72
	v_add_f32_e32 v84, v203, v72
	ds_read_b64_tr_b16 v[72:73], v213 offset:12416
	ds_read_b64_tr_b16 v[74:75], v214 offset:13184
	s_waitcnt lgkmcnt(2)
	v_mfma_f32_32x32x16_bf16 v[16:31], v[80:83], v[76:79], v[16:31]
	v_add_f32_e32 v76, v204, v84
	v_add_f32_e32 v76, v205, v76
	v_add_f32_e32 v76, v206, v76
	v_add_f32_e32 v76, v207, v76
	v_add_f32_e32 v80, v208, v76
	ds_read_b64_tr_b16 v[76:77], v213 offset:18560
	ds_read_b64_tr_b16 v[78:79], v214 offset:19328
	s_waitcnt vmcnt(0)
	s_waitcnt lgkmcnt(2)
	v_mfma_f32_32x32x16_bf16 v[16:31], v[72:75], v[68:71], v[16:31]
	v_add_f32_e32 v68, v211, v80
	v_add_f32_e32 v68, v212, v68
	v_mov_b32_e32 v69, v68
	s_nop 1
	v_permlane32_swap_b32_e32 v68, v69
	v_add_f32_e32 v158, v68, v69
	v_fmac_f32_e32 v158, v159, v146
	s_waitcnt lgkmcnt(0)
	v_mfma_f32_32x32x16_bf16 v[16:31], v[76:79], v[64:67], v[16:31]
	s_barrier
	s_cbranch_scc1 .LBB0_1250
	s_branch .LBB0_1238
.LBB0_1250:
	s_cmp_eq_u32 s101, 0
	s_cbranch_scc1 .Lg_done
	v_cmp_gt_f32_e32 vcc, 0x7149f2ca, v158
	s_mov_b64 s[16:17], vcc
	v_cmp_lt_f32_e32 vcc, 0x0da24260, v158
	s_and_b64 vcc, vcc, s[16:17]
	v_mov_b32_e32 v159, 0x20180
	s_cmp_eq_u64 vcc, exec
	s_cbranch_scc1 .Lg_vote
	v_mov_b32_e32 v160, 1
	ds_write_b32 v159, v160
.Lg_vote:
	s_waitcnt lgkmcnt(0)
	s_barrier
	ds_read_b32 v160, v159
	s_waitcnt lgkmcnt(0)
	v_readfirstlane_b32 s16, v160
	s_cmp_eq_u32 s16, 0
	s_cbranch_scc1 .Lg_done
	s_barrier
	v_mov_b32_e32 v160, 0
	ds_write_b32 v159, v160
	s_waitcnt lgkmcnt(0)
	s_mov_b32 s99, 1
	s_mov_b32 s6, s100
	s_cmp_eq_u32 s100, 0
	s_cselect_b64 s[4:5], -1, 0
	v_readlane_b32 s62, v251, 12
	v_readlane_b32 s63, v251, 13
	s_nop 7
	s_load_dword s54, s[62:63], 0xc0
	s_branch .LBB0_1216
.Lg_done:
	s_mov_b32 s99, 0
	v_ashrrev_i32_e32 v74, 4, v202
	v_lshlrev_b32_e32 v180, 4, v201
	v_ashrrev_i32_e32 v75, 31, v74
	v_lshl_add_u64 v[70:71], s[52:53], 0, v[180:181]
	v_lshlrev_b64 v[64:65], 8, v[74:75]
	v_lshl_add_u64 v[64:65], v[70:71], 0, v[64:65]
	global_load_dwordx4 v[64:67], v[64:65], off
	v_add_u32_e32 v204, 0x200, v202
	v_ashrrev_i32_e32 v76, 4, v204
	v_ashrrev_i32_e32 v77, 31, v76
	v_lshlrev_b64 v[204:205], 8, v[76:77]
	v_lshl_add_u64 v[204:205], v[70:71], 0, v[204:205]
	global_load_dwordx4 v[204:207], v[204:205], off
	v_add_u32_e32 v208, 0x400, v202
	v_ashrrev_i32_e32 v78, 4, v208
	v_ashrrev_i32_e32 v79, 31, v78
	v_lshlrev_b64 v[208:209], 8, v[78:79]
	v_lshl_add_u64 v[208:209], v[70:71], 0, v[208:209]
	global_load_dwordx4 v[208:211], v[208:209], off
	v_add_u32_e32 v212, 0x600, v202
	v_ashrrev_i32_e32 v80, 4, v212
	v_ashrrev_i32_e32 v81, 31, v80
	v_lshlrev_b64 v[212:213], 8, v[80:81]
	v_lshl_add_u64 v[212:213], v[70:71], 0, v[212:213]
	global_load_dwordx4 v[212:215], v[212:213], off
	s_mul_i32 s4, s67, 0xc00
	s_mul_hi_u32 s5, s66, 0xc00
	s_add_i32 s5, s5, s4
	s_mul_i32 s4, s66, 0xc00
	s_add_u32 s20, s80, s4
	v_add_u32_e32 v72, 0, v180
	s_addc_u32 s7, s81, s5
	v_mad_u64_u32 v[74:75], s[4:5], v74, s1, v[72:73]
	v_rcp_f32_e32 v68, v158
	s_and_b32 s21, s7, 0xffff
	s_and_b64 vcc, exec, s[62:63]
	v_readlane_b32 s62, v251, 12
	v_pk_mul_f32 v[48:49], v[68:69], v[48:49] op_sel_hi:[0,1]
	v_pk_mul_f32 v[32:33], v[68:69], v[32:33] op_sel_hi:[0,1]
	v_pk_mul_f32 v[0:1], v[68:69], v[0:1] op_sel_hi:[0,1]
	v_readlane_b32 s63, v251, 13
	s_waitcnt vmcnt(3)
	ds_write_b128 v74, v[64:67]
	v_mad_u64_u32 v[74:75], s[4:5], v76, s1, v[72:73]
	s_waitcnt vmcnt(2)
	ds_write_b128 v74, v[204:207]
	v_mad_u64_u32 v[74:75], s[4:5], v78, s1, v[72:73]
	s_waitcnt vmcnt(1)
	ds_write_b128 v74, v[208:211]
	v_mad_u64_u32 v[70:71], s[4:5], v80, s1, v[72:73]
	s_waitcnt vmcnt(0)
	ds_write_b128 v70, v[212:215]
	v_cvt_pk_bf16_f32 v64, v48, v49
	v_pk_mul_f32 v[48:49], v[68:69], v[50:51] op_sel_hi:[0,1]
	v_cvt_pk_bf16_f32 v65, v48, v49
	v_pk_mul_f32 v[48:49], v[68:69], v[52:53] op_sel_hi:[0,1]
	v_cvt_pk_bf16_f32 v66, v48, v49
	v_pk_mul_f32 v[48:49], v[68:69], v[54:55] op_sel_hi:[0,1]
	v_cvt_pk_bf16_f32 v52, v32, v33
	v_pk_mul_f32 v[32:33], v[68:69], v[34:35] op_sel_hi:[0,1]
	v_cvt_pk_bf16_f32 v67, v48, v49
	v_pk_mul_f32 v[48:49], v[68:69], v[56:57] op_sel_hi:[0,1]
	v_cvt_pk_bf16_f32 v53, v32, v33
	v_pk_mul_f32 v[32:33], v[68:69], v[36:37] op_sel_hi:[0,1]
	v_cvt_pk_bf16_f32 v56, v48, v49
	v_pk_mul_f32 v[48:49], v[68:69], v[58:59] op_sel_hi:[0,1]
	v_cvt_pk_bf16_f32 v54, v32, v33
	v_pk_mul_f32 v[32:33], v[68:69], v[38:39] op_sel_hi:[0,1]
	v_cvt_pk_bf16_f32 v57, v48, v49
	v_pk_mul_f32 v[48:49], v[68:69], v[60:61] op_sel_hi:[0,1]
	v_cvt_pk_bf16_f32 v55, v32, v33
	v_pk_mul_f32 v[32:33], v[68:69], v[40:41] op_sel_hi:[0,1]
	v_cvt_pk_bf16_f32 v40, v0, v1
	v_pk_mul_f32 v[0:1], v[68:69], v[2:3] op_sel_hi:[0,1]
	v_cvt_pk_bf16_f32 v58, v48, v49
	v_pk_mul_f32 v[48:49], v[68:69], v[62:63] op_sel_hi:[0,1]
	v_cvt_pk_bf16_f32 v41, v0, v1
	v_pk_mul_f32 v[0:1], v[68:69], v[4:5] op_sel_hi:[0,1]
	v_cvt_pk_bf16_f32 v59, v48, v49
	v_cvt_pk_bf16_f32 v48, v32, v33
	v_pk_mul_f32 v[32:33], v[68:69], v[42:43] op_sel_hi:[0,1]
	v_cvt_pk_bf16_f32 v42, v0, v1
	v_pk_mul_f32 v[0:1], v[68:69], v[6:7] op_sel_hi:[0,1]
	v_cvt_pk_bf16_f32 v43, v0, v1
	v_pk_mul_f32 v[0:1], v[68:69], v[8:9] op_sel_hi:[0,1]
	v_cvt_pk_bf16_f32 v36, v0, v1
	v_pk_mul_f32 v[0:1], v[68:69], v[10:11] op_sel_hi:[0,1]
	v_cvt_pk_bf16_f32 v37, v0, v1
	v_pk_mul_f32 v[0:1], v[68:69], v[12:13] op_sel_hi:[0,1]
	v_cvt_pk_bf16_f32 v49, v32, v33
	v_pk_mul_f32 v[32:33], v[68:69], v[44:45] op_sel_hi:[0,1]
	v_cvt_pk_bf16_f32 v38, v0, v1
	v_pk_mul_f32 v[0:1], v[68:69], v[14:15] op_sel_hi:[0,1]
	v_cvt_pk_bf16_f32 v50, v32, v33
	v_pk_mul_f32 v[32:33], v[68:69], v[46:47] op_sel_hi:[0,1]
	v_cvt_pk_bf16_f32 v39, v0, v1
	v_pk_mul_f32 v[0:1], v[68:69], v[16:17] op_sel_hi:[0,1]
	v_cvt_pk_bf16_f32 v51, v32, v33
	v_cvt_pk_bf16_f32 v32, v0, v1
	v_pk_mul_f32 v[0:1], v[68:69], v[18:19] op_sel_hi:[0,1]
	v_cvt_pk_bf16_f32 v33, v0, v1
	v_pk_mul_f32 v[0:1], v[68:69], v[20:21] op_sel_hi:[0,1]
	v_cvt_pk_bf16_f32 v34, v0, v1
	v_pk_mul_f32 v[0:1], v[68:69], v[22:23] op_sel_hi:[0,1]
	v_cvt_pk_bf16_f32 v35, v0, v1
	v_pk_mul_f32 v[0:1], v[68:69], v[24:25] op_sel_hi:[0,1]
	v_cvt_pk_bf16_f32 v16, v0, v1
	v_pk_mul_f32 v[0:1], v[68:69], v[26:27] op_sel_hi:[0,1]
	v_cvt_pk_bf16_f32 v17, v0, v1
	v_pk_mul_f32 v[0:1], v[68:69], v[28:29] op_sel_hi:[0,1]
	v_cvt_pk_bf16_f32 v18, v0, v1
	v_pk_mul_f32 v[0:1], v[68:69], v[30:31] op_sel_hi:[0,1]
	v_cvt_pk_bf16_f32 v19, v0, v1
	v_mul_u32_u24_e32 v0, 0x600, v200
	v_or_b32_e32 v20, v145, v0
	v_mul_u32_u24_e32 v0, 0x110, v200
	v_add3_u32 v21, 0, v169, v0
	s_waitcnt lgkmcnt(0)
	s_barrier
	v_lshlrev_b32_e32 v20, 1, v20
	v_add_u32_e32 v26, 0x2000, v21
	v_add_u32_e32 v27, 0x4000, v21
	v_add_u32_e32 v28, 0x6000, v21
	ds_read2_b64 v[76:79], v21 offset1:2
	ds_read2_b64 v[80:83], v21 offset0:4 offset1:6
	ds_read2_b64 v[84:87], v21 offset0:8 offset1:10
	ds_read2_b64 v[88:91], v21 offset0:12 offset1:14
	ds_read2_b64 v[92:95], v21 offset0:16 offset1:18
	ds_read2_b64 v[160:163], v21 offset0:20 offset1:22
	ds_read2_b64 v[164:167], v21 offset0:24 offset1:26
	ds_read2_b64 v[176:179], v21 offset0:28 offset1:30
	ds_read2_b64 v[204:207], v26 offset0:64 offset1:66
	ds_read2_b64 v[208:211], v26 offset0:68 offset1:70
	ds_read2_b64 v[212:215], v26 offset0:72 offset1:74
	ds_read2_b64 v[216:219], v26 offset0:76 offset1:78
	ds_read2_b64 v[220:223], v26 offset0:80 offset1:82
	ds_read2_b64 v[22:25], v26 offset0:84 offset1:86
	ds_read2_b64 v[68:71], v26 offset0:88 offset1:90
	ds_read2_b64 v[72:75], v26 offset0:92 offset1:94
	s_waitcnt lgkmcnt(8)
	v_mfma_f32_32x32x16_bf16 v[0:15], v[76:79], v[64:67], 0
	v_mfma_f32_32x32x16_bf16 v[0:15], v[80:83], v[56:59], v[0:15]
	v_mfma_f32_32x32x16_bf16 v[0:15], v[84:87], v[52:55], v[0:15]
	v_mfma_f32_32x32x16_bf16 v[0:15], v[88:91], v[48:51], v[0:15]
	v_mfma_f32_32x32x16_bf16 v[0:15], v[92:95], v[40:43], v[0:15]
	v_mfma_f32_32x32x16_bf16 v[0:15], v[160:163], v[36:39], v[0:15]
	v_mfma_f32_32x32x16_bf16 v[0:15], v[164:167], v[32:35], v[0:15]
	v_mfma_f32_32x32x16_bf16 v[0:15], v[176:179], v[16:19], v[0:15]
	ds_read2_b64 v[76:79], v27 offset0:128 offset1:130
	ds_read2_b64 v[80:83], v27 offset0:132 offset1:134
	ds_read2_b64 v[84:87], v27 offset0:136 offset1:138
	ds_read2_b64 v[88:91], v27 offset0:140 offset1:142
	ds_read2_b64 v[92:95], v27 offset0:144 offset1:146
	ds_read2_b64 v[160:163], v27 offset0:148 offset1:150
	ds_read2_b64 v[164:167], v27 offset0:152 offset1:154
	ds_read2_b64 v[176:179], v27 offset0:156 offset1:158
	s_nop 11
	v_cvt_pk_bf16_f32 v0, v0, v1
	v_cvt_pk_bf16_f32 v1, v2, v3
	buffer_store_dwordx2 v[0:1], v20, s[20:23], 0 offen sc1
	v_cvt_pk_bf16_f32 v0, v4, v5
	v_cvt_pk_bf16_f32 v1, v6, v7
	buffer_store_dwordx2 v[0:1], v20, s[20:23], 0 offen offset:16 sc1
	v_cvt_pk_bf16_f32 v0, v8, v9
	v_cvt_pk_bf16_f32 v1, v10, v11
	buffer_store_dwordx2 v[0:1], v20, s[20:23], 0 offen offset:32 sc1
	v_cvt_pk_bf16_f32 v0, v12, v13
	v_cvt_pk_bf16_f32 v1, v14, v15
	buffer_store_dwordx2 v[0:1], v20, s[20:23], 0 offen offset:48 sc1
	s_waitcnt lgkmcnt(8)
	v_mfma_f32_32x32x16_bf16 v[0:15], v[204:207], v[64:67], 0
	v_mfma_f32_32x32x16_bf16 v[0:15], v[208:211], v[56:59], v[0:15]
	v_mfma_f32_32x32x16_bf16 v[0:15], v[212:215], v[52:55], v[0:15]
	v_mfma_f32_32x32x16_bf16 v[0:15], v[216:219], v[48:51], v[0:15]
	v_mfma_f32_32x32x16_bf16 v[0:15], v[220:223], v[40:43], v[0:15]
	v_mfma_f32_32x32x16_bf16 v[0:15], v[22:25], v[36:39], v[0:15]
	v_mfma_f32_32x32x16_bf16 v[0:15], v[68:71], v[32:35], v[0:15]
	v_mfma_f32_32x32x16_bf16 v[0:15], v[72:75], v[16:19], v[0:15]
	ds_read2_b64 v[204:207], v28 offset0:192 offset1:194
	ds_read2_b64 v[208:211], v28 offset0:196 offset1:198
	ds_read2_b64 v[212:215], v28 offset0:200 offset1:202
	ds_read2_b64 v[216:219], v28 offset0:204 offset1:206
	ds_read2_b64 v[220:223], v28 offset0:208 offset1:210
	ds_read2_b64 v[22:25], v28 offset0:212 offset1:214
	ds_read2_b64 v[68:71], v28 offset0:216 offset1:218
	ds_read2_b64 v[72:75], v28 offset0:220 offset1:222
	s_nop 11
	v_cvt_pk_bf16_f32 v0, v0, v1
	v_cvt_pk_bf16_f32 v1, v2, v3
	buffer_store_dwordx2 v[0:1], v20, s[20:23], 0 offen offset:64 sc1
	v_cvt_pk_bf16_f32 v0, v4, v5
	v_cvt_pk_bf16_f32 v1, v6, v7
	buffer_store_dwordx2 v[0:1], v20, s[20:23], 0 offen offset:80 sc1
	v_cvt_pk_bf16_f32 v0, v8, v9
	v_cvt_pk_bf16_f32 v1, v10, v11
	buffer_store_dwordx2 v[0:1], v20, s[20:23], 0 offen offset:96 sc1
	v_cvt_pk_bf16_f32 v0, v12, v13
	v_cvt_pk_bf16_f32 v1, v14, v15
	buffer_store_dwordx2 v[0:1], v20, s[20:23], 0 offen offset:112 sc1
	s_waitcnt lgkmcnt(8)
	v_mfma_f32_32x32x16_bf16 v[0:15], v[76:79], v[64:67], 0
	v_mfma_f32_32x32x16_bf16 v[0:15], v[80:83], v[56:59], v[0:15]
	v_mfma_f32_32x32x16_bf16 v[0:15], v[84:87], v[52:55], v[0:15]
	v_mfma_f32_32x32x16_bf16 v[0:15], v[88:91], v[48:51], v[0:15]
	v_mfma_f32_32x32x16_bf16 v[0:15], v[92:95], v[40:43], v[0:15]
	v_mfma_f32_32x32x16_bf16 v[0:15], v[160:163], v[36:39], v[0:15]
	v_mfma_f32_32x32x16_bf16 v[0:15], v[164:167], v[32:35], v[0:15]
	v_mfma_f32_32x32x16_bf16 v[0:15], v[176:179], v[16:19], v[0:15]
	s_nop 11
	v_cvt_pk_bf16_f32 v0, v0, v1
	v_cvt_pk_bf16_f32 v1, v2, v3
	buffer_store_dwordx2 v[0:1], v20, s[20:23], 0 offen offset:128 sc1
	v_cvt_pk_bf16_f32 v0, v4, v5
	v_cvt_pk_bf16_f32 v1, v6, v7
	buffer_store_dwordx2 v[0:1], v20, s[20:23], 0 offen offset:144 sc1
	v_cvt_pk_bf16_f32 v0, v8, v9
	v_cvt_pk_bf16_f32 v1, v10, v11
	buffer_store_dwordx2 v[0:1], v20, s[20:23], 0 offen offset:160 sc1
	v_cvt_pk_bf16_f32 v0, v12, v13
	v_cvt_pk_bf16_f32 v1, v14, v15
	buffer_store_dwordx2 v[0:1], v20, s[20:23], 0 offen offset:176 sc1
	s_waitcnt lgkmcnt(0)
	v_mfma_f32_32x32x16_bf16 v[0:15], v[204:207], v[64:67], 0
	v_mfma_f32_32x32x16_bf16 v[0:15], v[208:211], v[56:59], v[0:15]
	v_mfma_f32_32x32x16_bf16 v[0:15], v[212:215], v[52:55], v[0:15]
	v_mfma_f32_32x32x16_bf16 v[0:15], v[216:219], v[48:51], v[0:15]
	v_mfma_f32_32x32x16_bf16 v[0:15], v[220:223], v[40:43], v[0:15]
	v_mfma_f32_32x32x16_bf16 v[0:15], v[22:25], v[36:39], v[0:15]
	v_mfma_f32_32x32x16_bf16 v[0:15], v[68:71], v[32:35], v[0:15]
	v_mfma_f32_32x32x16_bf16 v[0:15], v[72:75], v[16:19], v[0:15]
	s_nop 11
	v_cvt_pk_bf16_f32 v0, v0, v1
	v_cvt_pk_bf16_f32 v1, v2, v3
	buffer_store_dwordx2 v[0:1], v20, s[20:23], 0 offen offset:192 sc1
	v_cvt_pk_bf16_f32 v0, v4, v5
	v_cvt_pk_bf16_f32 v1, v6, v7
	buffer_store_dwordx2 v[0:1], v20, s[20:23], 0 offen offset:208 sc1
	v_cvt_pk_bf16_f32 v0, v8, v9
	v_cvt_pk_bf16_f32 v1, v10, v11
	buffer_store_dwordx2 v[0:1], v20, s[20:23], 0 offen offset:224 sc1
	v_cvt_pk_bf16_f32 v0, v12, v13
	v_cvt_pk_bf16_f32 v1, v14, v15
	buffer_store_dwordx2 v[0:1], v20, s[20:23], 0 offen offset:240 sc1
	s_cbranch_vccz .LBB0_1339
	s_lshl_b32 s8, s8, 6
	s_ashr_i32 s9, s8, 31
	s_cmp_eq_u64 s[64:65], 0
	s_cbranch_scc1 .LBB0_1253
	s_lshl_b64 s[4:5], s[8:9], 2
	s_add_u32 s4, s64, s4
	s_addc_u32 s5, s65, s5
	v_lshlrev_b32_e32 v4, 2, v182
	global_load_dwordx4 v[0:3], v4, s[4:5] offset:16
	s_nop 0
	global_load_dwordx4 v[4:7], v4, s[4:5]
	s_branch .LBB0_1254
